# v46 + 24 provably redundant s_waitcnt lgkmcnt(0) (second wait right after barrier+setprio) deleted from the GEMM K-loops of P2/P4/P5/P7/P8
# baseline (speedup 1.0000x reference)
; #define PG8_STAGE(bufoff, gbase, voff) do { _Pragma("unroll") for (int _i = 0; _i < 2; ++_i) \
;         __builtin_amdgcn_global_load_lds((const unsigned*)((const char*)(gbase) + (voff)[_i]), (LAS unsigned*)(lds + (bufoff) + ldsw + _i * 8192), 16, 0, 0); } while (0)
; #define PG8_LDA(dst, b, h) do { _Pragma("unroll") for (int m = 0; m < 4; ++m) { if constexpr (F8) dst##8[m] = PG8_LD32(lds + PG8_SA(b, h) + aoff + m * 2048); \
;         else { _Pragma("unroll") for (int k = 0; k < 2; ++k) dst[m][k] = *(const LAS bf16x8*)(lds + PG8_SA(b, h) + aoff + m * 2048 + k * 1024); } } } while (0)
; #define PG8_LDB(dst, b, h) do { _Pragma("unroll") for (int n = 0; n < 2; ++n) { if constexpr (F8) dst##8[n] = PG8_LD32(lds + PG8_SB(b, h) + boff + n * 2048); \
;         else { _Pragma("unroll") for (int k = 0; k < 2; ++k) dst[n][k] = *(const LAS bf16x8*)(lds + PG8_SB(b, h) + boff + n * 2048 + k * 1024); } } } while (0)
; #define PG8_WAIT_V(n) asm volatile("s_waitcnt vmcnt(" #n ")" ::: "memory")
; #define PG8_WAIT_L(n) asm volatile("s_waitcnt lgkmcnt(" #n ")" ::: "memory")
; #define PG8_BAR __builtin_amdgcn_s_barrier()
; #define PG8_SCHED __builtin_amdgcn_sched_barrier(0)
; template <class Epi, class Sched, bool GATHER, bool F8 = false>
; __device__ __forceinline__ void gemm_phase(LAS unsigned char* lds, const int K, const Sched& S, const Epi& E) {
;     ...
;         for (int t = 0; t < nt; t += 2) {
;             const bool last = (t == nt - 2);
;             const char* a1 = cA + (size_t)(t + 1) * kstep;
;             const char* a2 = last ? nA : cA + (size_t)(t + 2) * kstep; const char* b2 = last ? nB : cB + (size_t)(t + 2) * kstep;
;             const char* a3 = a2 + kstep; const char* b3 = b2 + kstep;
;             if constexpr (GATHER) { if (last && has_next) S.offsets(ui + 1, RA, CA, vN); }
;             PG8_LDB(B0, 0, 0); PG8_LDB(B1, 0, 1); PG8_SCHED; PG8_LDA(At, 0, 0); PG8_STAGE(PG8_SA(1, 1), a1, vA[1]);
;             PG8_WAIT_V(8); PG8_WAIT_L(0); PG8_BAR; PG8_MMA(0, 0, At, B0); PG8_MMA(0, 1, At, B1); PG8_BAR; PG8_SCHED;
;             PG8_LDA(At, 0, 1); PG8_STAGE(PG8_SB(0, 0), b2, voffB); PG8_STAGE(PG8_SB(0, 1), b2 + hstepB, voffB); PG8_STAGE(PG8_SA(0, 0), a2, vN[0]);
;             PG8_WAIT_V(8); PG8_WAIT_L(0); PG8_BAR; PG8_MMA(1, 0, At, B0); PG8_MMA(1, 1, At, B1); PG8_BAR; PG8_SCHED;
.LBB0_265:
	ds_read_b128 v[182:185], v177
	ds_read_b128 v[186:189], v177 offset:1024
	ds_read_b128 v[190:193], v177 offset:2048
	ds_read_b128 v[194:197], v177 offset:3072
	ds_read_b128 v[198:201], v178
	ds_read_b128 v[202:205], v178 offset:1024
	ds_read_b128 v[206:209], v178 offset:2048
	ds_read_b128 v[210:213], v178 offset:3072
	s_add_u32 s44, s0, 0x80
	s_addc_u32 s45, s1, 0
	s_cmp_eq_u32 vcc_lo, 28
	s_cselect_b32 s67, s49, s45
	s_cselect_b32 s66, s48, s44
	s_cselect_b32 s65, s63, s92
	s_cselect_b32 s64, s62, s12
	v_lshl_add_u64 v[246:247], s[0:1], 0, v[154:155]
	s_add_i32 m0, s72, 0xc000
	ds_read_b128 v[214:217], v179
	ds_read_b128 v[218:221], v179 offset:1024
	ds_read_b128 v[222:225], v179 offset:2048
	ds_read_b128 v[226:229], v179 offset:3072
	ds_read_b128 v[230:233], v179 offset:4096
	ds_read_b128 v[234:237], v179 offset:5120
	ds_read_b128 v[238:241], v179 offset:6144
	ds_read_b128 v[242:245], v179 offset:7168
	global_load_lds_dwordx4 v[246:247], off
	v_lshl_add_u64 v[246:247], s[0:1], 0, v[156:157]
	s_add_i32 m0, s72, 0xe000
	s_nop 0
	global_load_lds_dwordx4 v[246:247], off
	s_waitcnt vmcnt(8)
	s_waitcnt lgkmcnt(0)
	s_barrier
	s_setprio 1
	v_mfma_f32_16x16x32_bf16 v[126:129], v[182:185], v[214:217], v[126:129]
	v_mfma_f32_16x16x32_bf16 v[122:125], v[190:193], v[214:217], v[122:125]
	v_mfma_f32_16x16x32_bf16 v[110:113], v[182:185], v[222:225], v[110:113]
	v_mfma_f32_16x16x32_bf16 v[106:109], v[190:193], v[222:225], v[106:109]
	v_mfma_f32_16x16x32_bf16 v[94:97], v[182:185], v[230:233], v[94:97]
	v_mfma_f32_16x16x32_bf16 v[90:93], v[190:193], v[230:233], v[90:93]
	v_mfma_f32_16x16x32_bf16 v[78:81], v[182:185], v[238:241], v[78:81]
	v_mfma_f32_16x16x32_bf16 v[74:77], v[190:193], v[238:241], v[74:77]
	v_mfma_f32_16x16x32_bf16 v[126:129], v[186:189], v[218:221], v[126:129]
	v_mfma_f32_16x16x32_bf16 v[122:125], v[194:197], v[218:221], v[122:125]
	v_mfma_f32_16x16x32_bf16 v[110:113], v[186:189], v[226:229], v[110:113]
	v_mfma_f32_16x16x32_bf16 v[106:109], v[194:197], v[226:229], v[106:109]
	v_mfma_f32_16x16x32_bf16 v[94:97], v[186:189], v[234:237], v[94:97]
	v_mfma_f32_16x16x32_bf16 v[90:93], v[194:197], v[234:237], v[90:93]
	v_mfma_f32_16x16x32_bf16 v[78:81], v[186:189], v[242:245], v[78:81]
	v_mfma_f32_16x16x32_bf16 v[74:77], v[194:197], v[242:245], v[74:77]
	s_setprio 0
	s_setprio 1
	v_mfma_f32_16x16x32_bf16 v[118:121], v[198:201], v[214:217], v[118:121]
	v_mfma_f32_16x16x32_bf16 v[114:117], v[206:209], v[214:217], v[114:117]
	v_mfma_f32_16x16x32_bf16 v[102:105], v[198:201], v[222:225], v[102:105]
	v_mfma_f32_16x16x32_bf16 v[98:101], v[206:209], v[222:225], v[98:101]
	v_mfma_f32_16x16x32_bf16 v[86:89], v[198:201], v[230:233], v[86:89]
	v_mfma_f32_16x16x32_bf16 v[82:85], v[206:209], v[230:233], v[82:85]
	v_mfma_f32_16x16x32_bf16 v[70:73], v[198:201], v[238:241], v[70:73]
	v_mfma_f32_16x16x32_bf16 v[66:69], v[206:209], v[238:241], v[66:69]
	v_mfma_f32_16x16x32_bf16 v[118:121], v[202:205], v[218:221], v[118:121]
	v_mfma_f32_16x16x32_bf16 v[114:117], v[210:213], v[218:221], v[114:117]
	v_mfma_f32_16x16x32_bf16 v[102:105], v[202:205], v[226:229], v[102:105]
	v_mfma_f32_16x16x32_bf16 v[98:101], v[210:213], v[226:229], v[98:101]
	v_mfma_f32_16x16x32_bf16 v[86:89], v[202:205], v[234:237], v[86:89]
	v_mfma_f32_16x16x32_bf16 v[82:85], v[210:213], v[234:237], v[82:85]
	v_mfma_f32_16x16x32_bf16 v[70:73], v[202:205], v[242:245], v[70:73]
	v_mfma_f32_16x16x32_bf16 v[66:69], v[210:213], v[242:245], v[66:69]
	s_setprio 0
	s_barrier
	s_add_i32 s44, s90, s71
	v_lshl_add_u64 v[246:247], s[64:65], 0, v[130:131]
	s_mov_b32 m0, s44
	ds_read_b128 v[214:217], v179 offset:16384
	ds_read_b128 v[218:221], v179 offset:17408
	ds_read_b128 v[222:225], v179 offset:18432
	ds_read_b128 v[226:229], v179 offset:19456
	ds_read_b128 v[230:233], v179 offset:20480
	ds_read_b128 v[234:237], v179 offset:21504
	ds_read_b128 v[238:241], v179 offset:22528
	ds_read_b128 v[242:245], v179 offset:23552
	global_load_lds_dwordx4 v[246:247], off
	s_add_i32 m0, s44, 0x2000
	s_add_u32 s84, s64, 0x20000
	v_lshl_add_u64 v[248:249], s[64:65], 0, v[136:137]
	s_addc_u32 s85, s65, 0
	s_add_i32 s44, s91, s71
	global_load_lds_dwordx4 v[248:249], off
	v_lshl_add_u64 v[250:251], s[84:85], 0, v[130:131]
	s_mov_b32 m0, s44
	v_lshl_add_u64 v[252:253], s[66:67], 0, v[138:139]
	global_load_lds_dwordx4 v[250:251], off
	v_lshl_add_u64 v[250:251], s[84:85], 0, v[136:137]
	s_add_i32 m0, s44, 0x2000
	s_nop 0
	global_load_lds_dwordx4 v[250:251], off
	v_lshl_add_u64 v[250:251], s[66:67], 0, v[132:133]
	s_mov_b32 m0, s72
	s_nop 0
	global_load_lds_dwordx4 v[250:251], off
	s_mov_b32 m0, s73
	s_nop 0
	global_load_lds_dwordx4 v[252:253], off
	s_waitcnt vmcnt(8)
	s_waitcnt lgkmcnt(0)
	s_barrier
; #define PG8_STAGE(bufoff, gbase, voff) do { _Pragma("unroll") for (int _i = 0; _i < 2; ++_i) \
;         __builtin_amdgcn_global_load_lds((const unsigned*)((const char*)(gbase) + (voff)[_i]), (LAS unsigned*)(lds + (bufoff) + ldsw + _i * 8192), 16, 0, 0); } while (0)
; #define PG8_LDA(dst, b, h) do { _Pragma("unroll") for (int m = 0; m < 4; ++m) { if constexpr (F8) dst##8[m] = PG8_LD32(lds + PG8_SA(b, h) + aoff + m * 2048); \
;         else { _Pragma("unroll") for (int k = 0; k < 2; ++k) dst[m][k] = *(const LAS bf16x8*)(lds + PG8_SA(b, h) + aoff + m * 2048 + k * 1024); } } } while (0)
; #define PG8_LDB(dst, b, h) do { _Pragma("unroll") for (int n = 0; n < 2; ++n) { if constexpr (F8) dst##8[n] = PG8_LD32(lds + PG8_SB(b, h) + boff + n * 2048); \
;         else { _Pragma("unroll") for (int k = 0; k < 2; ++k) dst[n][k] = *(const LAS bf16x8*)(lds + PG8_SB(b, h) + boff + n * 2048 + k * 1024); } } } while (0)
; #define PG8_WAIT_V(n) asm volatile("s_waitcnt vmcnt(" #n ")" ::: "memory")
; #define PG8_WAIT_L(n) asm volatile("s_waitcnt lgkmcnt(" #n ")" ::: "memory")
; #define PG8_BAR __builtin_amdgcn_s_barrier()
; #define PG8_SCHED __builtin_amdgcn_sched_barrier(0)
; template <class Epi, class Sched, bool GATHER, bool F8 = false>
; __device__ __forceinline__ void gemm_phase(LAS unsigned char* lds, const int K, const Sched& S, const Epi& E) {
;     ...
;             PG8_WAIT_V(8); PG8_WAIT_L(0); PG8_BAR; PG8_MMA(1, 0, At, B0); PG8_MMA(1, 1, At, B1); PG8_BAR; PG8_SCHED;
;             PG8_LDB(B0, 1, 0); PG8_LDB(B1, 1, 1); PG8_SCHED; PG8_LDA(At, 1, 0); PG8_STAGE(PG8_SA(0, 1), a2, vN[1]);
;             PG8_WAIT_V(8); PG8_WAIT_L(0); PG8_BAR; PG8_MMA(0, 0, At, B0); PG8_MMA(0, 1, At, B1); PG8_BAR; PG8_SCHED;
	s_setprio 1
	v_mfma_f32_16x16x32_bf16 v[62:65], v[182:185], v[214:217], v[62:65]
	v_mfma_f32_16x16x32_bf16 v[58:61], v[190:193], v[214:217], v[58:61]
	v_mfma_f32_16x16x32_bf16 v[46:49], v[182:185], v[222:225], v[46:49]
	v_mfma_f32_16x16x32_bf16 v[42:45], v[190:193], v[222:225], v[42:45]
	v_mfma_f32_16x16x32_bf16 v[30:33], v[182:185], v[230:233], v[30:33]
	v_mfma_f32_16x16x32_bf16 v[26:29], v[190:193], v[230:233], v[26:29]
	v_mfma_f32_16x16x32_bf16 v[14:17], v[182:185], v[238:241], v[14:17]
	v_mfma_f32_16x16x32_bf16 v[10:13], v[190:193], v[238:241], v[10:13]
	v_mfma_f32_16x16x32_bf16 v[62:65], v[186:189], v[218:221], v[62:65]
	v_mfma_f32_16x16x32_bf16 v[58:61], v[194:197], v[218:221], v[58:61]
	v_mfma_f32_16x16x32_bf16 v[46:49], v[186:189], v[226:229], v[46:49]
	v_mfma_f32_16x16x32_bf16 v[42:45], v[194:197], v[226:229], v[42:45]
	v_mfma_f32_16x16x32_bf16 v[30:33], v[186:189], v[234:237], v[30:33]
	v_mfma_f32_16x16x32_bf16 v[26:29], v[194:197], v[234:237], v[26:29]
	v_mfma_f32_16x16x32_bf16 v[14:17], v[186:189], v[242:245], v[14:17]
	v_mfma_f32_16x16x32_bf16 v[10:13], v[194:197], v[242:245], v[10:13]
	s_setprio 0
	s_setprio 1
	v_mfma_f32_16x16x32_bf16 v[54:57], v[198:201], v[214:217], v[54:57]
	v_mfma_f32_16x16x32_bf16 v[50:53], v[206:209], v[214:217], v[50:53]
	v_mfma_f32_16x16x32_bf16 v[38:41], v[198:201], v[222:225], v[38:41]
	v_mfma_f32_16x16x32_bf16 v[34:37], v[206:209], v[222:225], v[34:37]
	v_mfma_f32_16x16x32_bf16 v[22:25], v[198:201], v[230:233], v[22:25]
	v_mfma_f32_16x16x32_bf16 v[18:21], v[206:209], v[230:233], v[18:21]
	v_mfma_f32_16x16x32_bf16 v[6:9], v[198:201], v[238:241], v[6:9]
	v_mfma_f32_16x16x32_bf16 v[2:5], v[206:209], v[238:241], v[2:5]
	v_mfma_f32_16x16x32_bf16 v[54:57], v[202:205], v[218:221], v[54:57]
	v_mfma_f32_16x16x32_bf16 v[50:53], v[210:213], v[218:221], v[50:53]
	v_mfma_f32_16x16x32_bf16 v[38:41], v[202:205], v[226:229], v[38:41]
	v_mfma_f32_16x16x32_bf16 v[34:37], v[210:213], v[226:229], v[34:37]
	v_mfma_f32_16x16x32_bf16 v[22:25], v[202:205], v[234:237], v[22:25]
	v_mfma_f32_16x16x32_bf16 v[18:21], v[210:213], v[234:237], v[18:21]
	v_mfma_f32_16x16x32_bf16 v[6:9], v[202:205], v[242:245], v[6:9]
	v_mfma_f32_16x16x32_bf16 v[2:5], v[210:213], v[242:245], v[2:5]
	s_setprio 0
	s_barrier
	s_add_i32 s44, 0, 0x18000
	v_add_u32_e32 v142, s44, v166
	s_add_i32 s45, 0, 0x1c000
	ds_read_b128 v[182:185], v142
	ds_read_b128 v[186:189], v142 offset:1024
	ds_read_b128 v[190:193], v142 offset:2048
	ds_read_b128 v[194:197], v142 offset:3072
	v_add_u32_e32 v142, s45, v166
	ds_read_b128 v[198:201], v142
	ds_read_b128 v[202:205], v142 offset:1024
	ds_read_b128 v[206:209], v142 offset:2048
	ds_read_b128 v[210:213], v142 offset:3072
	s_mov_b32 m0, s74
	v_lshl_add_u64 v[158:159], s[66:67], 0, v[134:135]
	ds_read_b128 v[214:217], v179 offset:32768
	ds_read_b128 v[218:221], v179 offset:33792
	ds_read_b128 v[222:225], v179 offset:34816
	ds_read_b128 v[226:229], v179 offset:35840
	ds_read_b128 v[230:233], v179 offset:36864
	ds_read_b128 v[234:237], v179 offset:37888
	ds_read_b128 v[238:241], v179 offset:38912
	ds_read_b128 v[242:245], v179 offset:39936
	global_load_lds_dwordx4 v[158:159], off
	v_lshl_add_u64 v[158:159], s[66:67], 0, v[140:141]
	s_mov_b32 m0, s75
	s_nop 0
	global_load_lds_dwordx4 v[158:159], off
	s_waitcnt vmcnt(8)
	s_waitcnt lgkmcnt(0)
	s_barrier
	s_setprio 1
	v_mfma_f32_16x16x32_bf16 v[126:129], v[182:185], v[214:217], v[126:129]
	v_mfma_f32_16x16x32_bf16 v[122:125], v[190:193], v[214:217], v[122:125]
	v_mfma_f32_16x16x32_bf16 v[110:113], v[182:185], v[222:225], v[110:113]
	v_mfma_f32_16x16x32_bf16 v[106:109], v[190:193], v[222:225], v[106:109]
	v_mfma_f32_16x16x32_bf16 v[94:97], v[182:185], v[230:233], v[94:97]
	v_mfma_f32_16x16x32_bf16 v[90:93], v[190:193], v[230:233], v[90:93]
	v_mfma_f32_16x16x32_bf16 v[78:81], v[182:185], v[238:241], v[78:81]
	v_mfma_f32_16x16x32_bf16 v[74:77], v[190:193], v[238:241], v[74:77]
	v_mfma_f32_16x16x32_bf16 v[126:129], v[186:189], v[218:221], v[126:129]
	v_mfma_f32_16x16x32_bf16 v[122:125], v[194:197], v[218:221], v[122:125]
	v_mfma_f32_16x16x32_bf16 v[110:113], v[186:189], v[226:229], v[110:113]
	v_mfma_f32_16x16x32_bf16 v[106:109], v[194:197], v[226:229], v[106:109]
	v_mfma_f32_16x16x32_bf16 v[94:97], v[186:189], v[234:237], v[94:97]
	v_mfma_f32_16x16x32_bf16 v[90:93], v[194:197], v[234:237], v[90:93]
	v_mfma_f32_16x16x32_bf16 v[78:81], v[186:189], v[242:245], v[78:81]
	v_mfma_f32_16x16x32_bf16 v[74:77], v[194:197], v[242:245], v[74:77]
	s_setprio 0
	s_setprio 1
	v_mfma_f32_16x16x32_bf16 v[118:121], v[198:201], v[214:217], v[118:121]
	v_mfma_f32_16x16x32_bf16 v[114:117], v[206:209], v[214:217], v[114:117]
	v_mfma_f32_16x16x32_bf16 v[102:105], v[198:201], v[222:225], v[102:105]
	v_mfma_f32_16x16x32_bf16 v[98:101], v[206:209], v[222:225], v[98:101]
	v_mfma_f32_16x16x32_bf16 v[86:89], v[198:201], v[230:233], v[86:89]
	v_mfma_f32_16x16x32_bf16 v[82:85], v[206:209], v[230:233], v[82:85]
	v_mfma_f32_16x16x32_bf16 v[70:73], v[198:201], v[238:241], v[70:73]
	v_mfma_f32_16x16x32_bf16 v[66:69], v[206:209], v[238:241], v[66:69]
	v_mfma_f32_16x16x32_bf16 v[118:121], v[202:205], v[218:221], v[118:121]
	v_mfma_f32_16x16x32_bf16 v[114:117], v[210:213], v[218:221], v[114:117]
	v_mfma_f32_16x16x32_bf16 v[102:105], v[202:205], v[226:229], v[102:105]
	v_mfma_f32_16x16x32_bf16 v[98:101], v[210:213], v[226:229], v[98:101]
	v_mfma_f32_16x16x32_bf16 v[86:89], v[202:205], v[234:237], v[86:89]
	v_mfma_f32_16x16x32_bf16 v[82:85], v[210:213], v[234:237], v[82:85]
	v_mfma_f32_16x16x32_bf16 v[70:73], v[202:205], v[242:245], v[70:73]
	v_mfma_f32_16x16x32_bf16 v[66:69], v[210:213], v[242:245], v[66:69]
	s_setprio 0
	s_barrier
; #define PG8_STAGE(bufoff, gbase, voff) do { _Pragma("unroll") for (int _i = 0; _i < 2; ++_i) \
;         __builtin_amdgcn_global_load_lds((const unsigned*)((const char*)(gbase) + (voff)[_i]), (LAS unsigned*)(lds + (bufoff) + ldsw + _i * 8192), 16, 0, 0); } while (0)
; #define PG8_LDA(dst, b, h) do { _Pragma("unroll") for (int m = 0; m < 4; ++m) { if constexpr (F8) dst##8[m] = PG8_LD32(lds + PG8_SA(b, h) + aoff + m * 2048); \
;         else { _Pragma("unroll") for (int k = 0; k < 2; ++k) dst[m][k] = *(const LAS bf16x8*)(lds + PG8_SA(b, h) + aoff + m * 2048 + k * 1024); } } } while (0)
; #define PG8_WAIT_V(n) asm volatile("s_waitcnt vmcnt(" #n ")" ::: "memory")
; #define PG8_WAIT_L(n) asm volatile("s_waitcnt lgkmcnt(" #n ")" ::: "memory")
; #define PG8_BAR __builtin_amdgcn_s_barrier()
; #define PG8_SCHED __builtin_amdgcn_sched_barrier(0)
; template <class Epi, class Sched, bool GATHER, bool F8 = false>
; __device__ __forceinline__ void gemm_phase(LAS unsigned char* lds, const int K, const Sched& S, const Epi& E) {
;     ...
;             PG8_LDA(At, 1, 1); PG8_STAGE(PG8_SB(1, 0), b3, voffB); PG8_STAGE(PG8_SB(1, 1), b3 + hstepB, voffB); PG8_STAGE(PG8_SA(1, 0), a3, vN[0]);
;             PG8_WAIT_V(8); PG8_WAIT_L(0); PG8_BAR; PG8_MMA(1, 0, At, B0); PG8_MMA(1, 1, At, B1); PG8_BAR; PG8_SCHED;
;         }
;         if (wr == 0) PG8_BAR;
	s_add_i32 s44, s44, s71
	v_lshl_add_u64 v[158:159], v[246:247], 0, s[20:21]
	s_mov_b32 m0, s44
	ds_read_b128 v[214:217], v179 offset:49152
	ds_read_b128 v[218:221], v179 offset:50176
	ds_read_b128 v[222:225], v179 offset:51200
	ds_read_b128 v[226:229], v179 offset:52224
	ds_read_b128 v[230:233], v179 offset:53248
	ds_read_b128 v[234:237], v179 offset:54272
	ds_read_b128 v[238:241], v179 offset:55296
	ds_read_b128 v[242:245], v179 offset:56320
	global_load_lds_dwordx4 v[158:159], off
	s_add_i32 m0, s44, 0x2000
	s_add_u32 s64, s64, 0x20080
	v_lshl_add_u64 v[158:159], v[248:249], 0, s[20:21]
	s_addc_u32 s65, s65, 0
	s_add_i32 s44, s45, s71
	global_load_lds_dwordx4 v[158:159], off
	v_lshl_add_u64 v[158:159], s[64:65], 0, v[130:131]
	s_mov_b32 m0, s44
	s_nop 0
	global_load_lds_dwordx4 v[158:159], off
	v_lshl_add_u64 v[158:159], s[64:65], 0, v[136:137]
	s_add_i32 m0, s44, 0x2000
	s_nop 0
	global_load_lds_dwordx4 v[158:159], off
	v_lshl_add_u64 v[158:159], v[250:251], 0, s[20:21]
	s_mov_b32 m0, s77
	s_nop 0
	global_load_lds_dwordx4 v[158:159], off
	v_lshl_add_u64 v[158:159], v[252:253], 0, s[20:21]
	s_mov_b32 m0, s78
	s_nop 0
	global_load_lds_dwordx4 v[158:159], off
	s_waitcnt vmcnt(8)
	s_waitcnt lgkmcnt(0)
	s_barrier
	s_setprio 1
	v_mfma_f32_16x16x32_bf16 v[62:65], v[182:185], v[214:217], v[62:65]
	v_mfma_f32_16x16x32_bf16 v[58:61], v[190:193], v[214:217], v[58:61]
	v_mfma_f32_16x16x32_bf16 v[46:49], v[182:185], v[222:225], v[46:49]
	v_mfma_f32_16x16x32_bf16 v[42:45], v[190:193], v[222:225], v[42:45]
	v_mfma_f32_16x16x32_bf16 v[30:33], v[182:185], v[230:233], v[30:33]
	v_mfma_f32_16x16x32_bf16 v[26:29], v[190:193], v[230:233], v[26:29]
	v_mfma_f32_16x16x32_bf16 v[14:17], v[182:185], v[238:241], v[14:17]
	v_mfma_f32_16x16x32_bf16 v[10:13], v[190:193], v[238:241], v[10:13]
	v_mfma_f32_16x16x32_bf16 v[62:65], v[186:189], v[218:221], v[62:65]
	v_mfma_f32_16x16x32_bf16 v[58:61], v[194:197], v[218:221], v[58:61]
	v_mfma_f32_16x16x32_bf16 v[46:49], v[186:189], v[226:229], v[46:49]
	v_mfma_f32_16x16x32_bf16 v[42:45], v[194:197], v[226:229], v[42:45]
	v_mfma_f32_16x16x32_bf16 v[30:33], v[186:189], v[234:237], v[30:33]
	v_mfma_f32_16x16x32_bf16 v[26:29], v[194:197], v[234:237], v[26:29]
	v_mfma_f32_16x16x32_bf16 v[14:17], v[186:189], v[242:245], v[14:17]
	v_mfma_f32_16x16x32_bf16 v[10:13], v[194:197], v[242:245], v[10:13]
	s_setprio 0
	s_setprio 1
	v_mfma_f32_16x16x32_bf16 v[54:57], v[198:201], v[214:217], v[54:57]
	v_mfma_f32_16x16x32_bf16 v[50:53], v[206:209], v[214:217], v[50:53]
	v_mfma_f32_16x16x32_bf16 v[38:41], v[198:201], v[222:225], v[38:41]
	v_mfma_f32_16x16x32_bf16 v[34:37], v[206:209], v[222:225], v[34:37]
	v_mfma_f32_16x16x32_bf16 v[22:25], v[198:201], v[230:233], v[22:25]
	v_mfma_f32_16x16x32_bf16 v[18:21], v[206:209], v[230:233], v[18:21]
	v_mfma_f32_16x16x32_bf16 v[6:9], v[198:201], v[238:241], v[6:9]
	v_mfma_f32_16x16x32_bf16 v[2:5], v[206:209], v[238:241], v[2:5]
	v_mfma_f32_16x16x32_bf16 v[54:57], v[202:205], v[218:221], v[54:57]
	v_mfma_f32_16x16x32_bf16 v[50:53], v[210:213], v[218:221], v[50:53]
	v_mfma_f32_16x16x32_bf16 v[38:41], v[202:205], v[226:229], v[38:41]
	v_mfma_f32_16x16x32_bf16 v[34:37], v[210:213], v[226:229], v[34:37]
	v_mfma_f32_16x16x32_bf16 v[22:25], v[202:205], v[234:237], v[22:25]
	v_mfma_f32_16x16x32_bf16 v[18:21], v[210:213], v[234:237], v[18:21]
	v_mfma_f32_16x16x32_bf16 v[6:9], v[202:205], v[242:245], v[6:9]
	v_mfma_f32_16x16x32_bf16 v[2:5], v[210:213], v[242:245], v[2:5]
	s_setprio 0
	s_barrier
	s_add_i32 vcc_lo, vcc_lo, 2
	s_add_u32 s0, s0, 0x100
	s_addc_u32 s1, s1, 0
	s_add_u32 s12, s12, 0x100
	s_addc_u32 s92, s92, 0
	s_cmp_gt_u32 vcc_lo, 29
	s_cbranch_scc0 .LBB0_265
	s_and_b64 vcc, exec, s[24:25]
	s_cbranch_vccz .LBB0_268
	s_barrier

; #define PG8_STAGE(bufoff, gbase, voff) do { _Pragma("unroll") for (int _i = 0; _i < 2; ++_i) \
;         __builtin_amdgcn_global_load_lds((const unsigned*)((const char*)(gbase) + (voff)[_i]), (LAS unsigned*)(lds + (bufoff) + ldsw + _i * 8192), 16, 0, 0); } while (0)
; #define PG8_LDA(dst, b, h) do { _Pragma("unroll") for (int m = 0; m < 4; ++m) { if constexpr (F8) dst##8[m] = PG8_LD32(lds + PG8_SA(b, h) + aoff + m * 2048); \
;         else { _Pragma("unroll") for (int k = 0; k < 2; ++k) dst[m][k] = *(const LAS bf16x8*)(lds + PG8_SA(b, h) + aoff + m * 2048 + k * 1024); } } } while (0)
; #define PG8_LDB(dst, b, h) do { _Pragma("unroll") for (int n = 0; n < 2; ++n) { if constexpr (F8) dst##8[n] = PG8_LD32(lds + PG8_SB(b, h) + boff + n * 2048); \
;         else { _Pragma("unroll") for (int k = 0; k < 2; ++k) dst[n][k] = *(const LAS bf16x8*)(lds + PG8_SB(b, h) + boff + n * 2048 + k * 1024); } } } while (0)
; #define PG8_WAIT_V(n) asm volatile("s_waitcnt vmcnt(" #n ")" ::: "memory")
; #define PG8_WAIT_L(n) asm volatile("s_waitcnt lgkmcnt(" #n ")" ::: "memory")
; #define PG8_BAR __builtin_amdgcn_s_barrier()
; #define PG8_SCHED __builtin_amdgcn_sched_barrier(0)
; template <class Epi, class Sched, bool GATHER, bool F8 = false>
; __device__ __forceinline__ void gemm_phase(LAS unsigned char* lds, const int K, const Sched& S, const Epi& E) {
;     ...
;             PG8_LDB(B0, 0, 0); PG8_LDB(B1, 0, 1); PG8_SCHED; PG8_LDA(At, 0, 0); PG8_STAGE(PG8_SA(1, 1), a1, vA[1]);
;             PG8_WAIT_V(8); PG8_WAIT_L(0); PG8_BAR; PG8_MMA(0, 0, At, B0); PG8_MMA(0, 1, At, B1); PG8_BAR; PG8_SCHED;
;             PG8_LDA(At, 0, 1); PG8_STAGE(PG8_SB(0, 0), b2, voffB); PG8_STAGE(PG8_SB(0, 1), b2 + hstepB, voffB); PG8_STAGE(PG8_SA(0, 0), a2, vN[0]);
;             PG8_WAIT_V(8); PG8_WAIT_L(0); PG8_BAR; PG8_MMA(1, 0, At, B0); PG8_MMA(1, 1, At, B1); PG8_BAR; PG8_SCHED;
.LBB0_346:
	ds_read_b128 v[18:21], v1
	ds_read_b128 v[22:25], v1 offset:1024
	ds_read_b128 v[26:29], v1 offset:2048
	ds_read_b128 v[30:33], v1 offset:3072
	ds_read_b128 v[2:5], v207
	ds_read_b128 v[6:9], v207 offset:1024
	ds_read_b128 v[10:13], v207 offset:2048
	ds_read_b128 v[14:17], v207 offset:3072
	s_add_u32 s48, s46, 0x80
	s_addc_u32 s49, s47, 0
	s_cmp_eq_u32 s97, 12
	s_cselect_b32 s63, s86, s49
	s_cselect_b32 s62, s87, s48
	s_cselect_b32 s49, s91, s96
	s_cselect_b32 s48, s92, s95
	v_lshl_add_u64 v[236:237], s[46:47], 0, v[178:179]
	s_add_i32 m0, s66, 0xc000
	ds_read_b128 v[182:185], v208
	ds_read_b128 v[186:189], v208 offset:1024
	ds_read_b128 v[212:215], v208 offset:2048
	ds_read_b128 v[216:219], v208 offset:3072
	ds_read_b128 v[220:223], v208 offset:4096
	ds_read_b128 v[224:227], v208 offset:5120
	ds_read_b128 v[228:231], v208 offset:6144
	ds_read_b128 v[232:235], v208 offset:7168
	global_load_lds_dwordx4 v[236:237], off
	v_lshl_add_u64 v[236:237], s[46:47], 0, v[180:181]
	s_add_i32 m0, s66, 0xe000
	s_nop 0
	global_load_lds_dwordx4 v[236:237], off
	s_waitcnt vmcnt(8)
	s_waitcnt lgkmcnt(0)
	s_barrier
	s_setprio 1
	v_mfma_scale_f32_16x16x128_f8f6f4 v[158:161], v[18:25], v[182:189], v[158:161], v190, v190 op_sel_hi:[0,0,0]
	v_mfma_scale_f32_16x16x128_f8f6f4 v[154:157], v[26:33], v[182:189], v[154:157], v190, v190 op_sel_hi:[0,0,0]
	v_mfma_scale_f32_16x16x128_f8f6f4 v[142:145], v[18:25], v[212:219], v[142:145], v190, v190 op_sel_hi:[0,0,0]
	v_mfma_scale_f32_16x16x128_f8f6f4 v[138:141], v[26:33], v[212:219], v[138:141], v190, v190 op_sel_hi:[0,0,0]
	v_mfma_scale_f32_16x16x128_f8f6f4 v[126:129], v[18:25], v[220:227], v[126:129], v190, v190 op_sel_hi:[0,0,0]
	v_mfma_scale_f32_16x16x128_f8f6f4 v[122:125], v[26:33], v[220:227], v[122:125], v190, v190 op_sel_hi:[0,0,0]
	v_mfma_scale_f32_16x16x128_f8f6f4 v[110:113], v[18:25], v[228:235], v[110:113], v190, v190 op_sel_hi:[0,0,0]
	v_mfma_scale_f32_16x16x128_f8f6f4 v[106:109], v[26:33], v[228:235], v[106:109], v190, v190 op_sel_hi:[0,0,0]
	s_setprio 0
	s_setprio 1
	v_mfma_scale_f32_16x16x128_f8f6f4 v[150:153], v[2:9], v[182:189], v[150:153], v190, v190 op_sel_hi:[0,0,0]
	v_mfma_scale_f32_16x16x128_f8f6f4 v[146:149], v[10:17], v[182:189], v[146:149], v190, v190 op_sel_hi:[0,0,0]
	v_mfma_scale_f32_16x16x128_f8f6f4 v[134:137], v[2:9], v[212:219], v[134:137], v190, v190 op_sel_hi:[0,0,0]
	v_mfma_scale_f32_16x16x128_f8f6f4 v[130:133], v[10:17], v[212:219], v[130:133], v190, v190 op_sel_hi:[0,0,0]
	v_mfma_scale_f32_16x16x128_f8f6f4 v[118:121], v[2:9], v[220:227], v[118:121], v190, v190 op_sel_hi:[0,0,0]
	v_mfma_scale_f32_16x16x128_f8f6f4 v[114:117], v[10:17], v[220:227], v[114:117], v190, v190 op_sel_hi:[0,0,0]
	v_mfma_scale_f32_16x16x128_f8f6f4 v[102:105], v[2:9], v[228:235], v[102:105], v190, v190 op_sel_hi:[0,0,0]
	v_mfma_scale_f32_16x16x128_f8f6f4 v[98:101], v[10:17], v[228:235], v[98:101], v190, v190 op_sel_hi:[0,0,0]
	s_setprio 0
	s_barrier
	s_add_i32 s84, s77, s65
	v_lshl_add_u64 v[182:183], s[48:49], 0, v[162:163]
	s_mov_b32 m0, s84
	ds_read_b128 v[212:215], v208 offset:16384
	ds_read_b128 v[216:219], v208 offset:17408
	ds_read_b128 v[220:223], v208 offset:18432
	ds_read_b128 v[224:227], v208 offset:19456
	ds_read_b128 v[228:231], v208 offset:20480
	ds_read_b128 v[232:235], v208 offset:21504
	ds_read_b128 v[236:239], v208 offset:22528
	ds_read_b128 v[240:243], v208 offset:23552
	global_load_lds_dwordx4 v[182:183], off
	s_add_i32 m0, s84, 0x2000
	s_add_u32 s84, s48, 0x10000
	v_lshl_add_u64 v[184:185], s[48:49], 0, v[168:169]
	s_addc_u32 s85, s49, 0
	s_add_i32 s93, s78, s65
	global_load_lds_dwordx4 v[184:185], off
	v_lshl_add_u64 v[186:187], s[84:85], 0, v[162:163]
	s_mov_b32 m0, s93
	v_lshl_add_u64 v[188:189], s[62:63], 0, v[172:173]
	global_load_lds_dwordx4 v[186:187], off
	v_lshl_add_u64 v[186:187], s[84:85], 0, v[168:169]
	s_add_i32 m0, s93, 0x2000
	s_nop 0
	global_load_lds_dwordx4 v[186:187], off
	v_lshl_add_u64 v[186:187], s[62:63], 0, v[164:165]
	s_mov_b32 m0, s66
	s_nop 0
	global_load_lds_dwordx4 v[186:187], off
	s_mov_b32 m0, s67
	s_nop 0
	global_load_lds_dwordx4 v[188:189], off
	s_waitcnt vmcnt(8)
	s_waitcnt lgkmcnt(0)
	s_barrier
	s_setprio 1
	v_mfma_scale_f32_16x16x128_f8f6f4 v[94:97], v[18:25], v[212:219], v[94:97], v190, v190 op_sel_hi:[0,0,0]
	v_mfma_scale_f32_16x16x128_f8f6f4 v[90:93], v[26:33], v[212:219], v[90:93], v190, v190 op_sel_hi:[0,0,0]
	v_mfma_scale_f32_16x16x128_f8f6f4 v[78:81], v[18:25], v[220:227], v[78:81], v190, v190 op_sel_hi:[0,0,0]
	v_mfma_scale_f32_16x16x128_f8f6f4 v[74:77], v[26:33], v[220:227], v[74:77], v190, v190 op_sel_hi:[0,0,0]
	v_mfma_scale_f32_16x16x128_f8f6f4 v[62:65], v[18:25], v[228:235], v[62:65], v190, v190 op_sel_hi:[0,0,0]
	v_mfma_scale_f32_16x16x128_f8f6f4 v[58:61], v[26:33], v[228:235], v[58:61], v190, v190 op_sel_hi:[0,0,0]
	v_mfma_scale_f32_16x16x128_f8f6f4 v[46:49], v[18:25], v[236:243], v[46:49], v190, v190 op_sel_hi:[0,0,0]
	v_mfma_scale_f32_16x16x128_f8f6f4 v[42:45], v[26:33], v[236:243], v[42:45], v190, v190 op_sel_hi:[0,0,0]
	s_setprio 0
	s_setprio 1
	v_mfma_scale_f32_16x16x128_f8f6f4 v[86:89], v[2:9], v[212:219], v[86:89], v190, v190 op_sel_hi:[0,0,0]
	v_mfma_scale_f32_16x16x128_f8f6f4 v[82:85], v[10:17], v[212:219], v[82:85], v190, v190 op_sel_hi:[0,0,0]
	v_mfma_scale_f32_16x16x128_f8f6f4 v[70:73], v[2:9], v[220:227], v[70:73], v190, v190 op_sel_hi:[0,0,0]
	v_mfma_scale_f32_16x16x128_f8f6f4 v[66:69], v[10:17], v[220:227], v[66:69], v190, v190 op_sel_hi:[0,0,0]
	v_mfma_scale_f32_16x16x128_f8f6f4 v[54:57], v[2:9], v[228:235], v[54:57], v190, v190 op_sel_hi:[0,0,0]
	v_mfma_scale_f32_16x16x128_f8f6f4 v[50:53], v[10:17], v[228:235], v[50:53], v190, v190 op_sel_hi:[0,0,0]
	v_mfma_scale_f32_16x16x128_f8f6f4 v[38:41], v[2:9], v[236:243], v[38:41], v190, v190 op_sel_hi:[0,0,0]
	v_mfma_scale_f32_16x16x128_f8f6f4 v[34:37], v[10:17], v[236:243], v[34:37], v190, v190 op_sel_hi:[0,0,0]
	s_setprio 0
	s_barrier
; #define PG8_STAGE(bufoff, gbase, voff) do { _Pragma("unroll") for (int _i = 0; _i < 2; ++_i) \
;         __builtin_amdgcn_global_load_lds((const unsigned*)((const char*)(gbase) + (voff)[_i]), (LAS unsigned*)(lds + (bufoff) + ldsw + _i * 8192), 16, 0, 0); } while (0)
; #define PG8_LDA(dst, b, h) do { _Pragma("unroll") for (int m = 0; m < 4; ++m) { if constexpr (F8) dst##8[m] = PG8_LD32(lds + PG8_SA(b, h) + aoff + m * 2048); \
;         else { _Pragma("unroll") for (int k = 0; k < 2; ++k) dst[m][k] = *(const LAS bf16x8*)(lds + PG8_SA(b, h) + aoff + m * 2048 + k * 1024); } } } while (0)
; #define PG8_LDB(dst, b, h) do { _Pragma("unroll") for (int n = 0; n < 2; ++n) { if constexpr (F8) dst##8[n] = PG8_LD32(lds + PG8_SB(b, h) + boff + n * 2048); \
;         else { _Pragma("unroll") for (int k = 0; k < 2; ++k) dst[n][k] = *(const LAS bf16x8*)(lds + PG8_SB(b, h) + boff + n * 2048 + k * 1024); } } } while (0)
; #define PG8_WAIT_V(n) asm volatile("s_waitcnt vmcnt(" #n ")" ::: "memory")
; #define PG8_WAIT_L(n) asm volatile("s_waitcnt lgkmcnt(" #n ")" ::: "memory")
; #define PG8_BAR __builtin_amdgcn_s_barrier()
; #define PG8_SCHED __builtin_amdgcn_sched_barrier(0)
; template <class Epi, class Sched, bool GATHER, bool F8 = false>
; __device__ __forceinline__ void gemm_phase(LAS unsigned char* lds, const int K, const Sched& S, const Epi& E) {
;     ...
;             PG8_LDB(B0, 1, 0); PG8_LDB(B1, 1, 1); PG8_SCHED; PG8_LDA(At, 1, 0); PG8_STAGE(PG8_SA(0, 1), a2, vN[1]);
;             PG8_WAIT_V(8); PG8_WAIT_L(0); PG8_BAR; PG8_MMA(0, 0, At, B0); PG8_MMA(0, 1, At, B1); PG8_BAR; PG8_SCHED;
;             PG8_LDA(At, 1, 1); PG8_STAGE(PG8_SB(1, 0), b3, voffB); PG8_STAGE(PG8_SB(1, 1), b3 + hstepB, voffB); PG8_STAGE(PG8_SA(1, 0), a3, vN[0]);
;             PG8_WAIT_V(8); PG8_WAIT_L(0); PG8_BAR; PG8_MMA(1, 0, At, B0); PG8_MMA(1, 1, At, B1); PG8_BAR; PG8_SCHED;
;         }
;         if (wr == 0) PG8_BAR;
	s_add_i32 s84, 0, 0x18000
	s_add_i32 s85, 0, 0x1c000
	v_add_u32_e32 v14, s84, v171
	v_add_u32_e32 v30, s85, v171
	ds_read_b128 v[2:5], v14
	ds_read_b128 v[6:9], v14 offset:1024
	ds_read_b128 v[10:13], v14 offset:2048
	ds_read_b128 v[14:17], v14 offset:3072
	ds_read_b128 v[18:21], v30
	ds_read_b128 v[22:25], v30 offset:1024
	ds_read_b128 v[26:29], v30 offset:2048
	ds_read_b128 v[30:33], v30 offset:3072
	s_mov_b32 m0, s68
	v_lshl_add_u64 v[244:245], s[62:63], 0, v[166:167]
	ds_read_b128 v[212:215], v208 offset:32768
	ds_read_b128 v[216:219], v208 offset:33792
	ds_read_b128 v[220:223], v208 offset:34816
	ds_read_b128 v[224:227], v208 offset:35840
	ds_read_b128 v[228:231], v208 offset:36864
	ds_read_b128 v[232:235], v208 offset:37888
	ds_read_b128 v[236:239], v208 offset:38912
	ds_read_b128 v[240:243], v208 offset:39936
	global_load_lds_dwordx4 v[244:245], off
	v_lshl_add_u64 v[244:245], s[62:63], 0, v[174:175]
	s_mov_b32 m0, s69
	s_nop 0
	global_load_lds_dwordx4 v[244:245], off
	s_waitcnt vmcnt(8)
	s_waitcnt lgkmcnt(0)
	s_barrier
	s_setprio 1
	v_mfma_scale_f32_16x16x128_f8f6f4 v[158:161], v[2:9], v[212:219], v[158:161], v190, v190 op_sel_hi:[0,0,0]
	v_mfma_scale_f32_16x16x128_f8f6f4 v[154:157], v[10:17], v[212:219], v[154:157], v190, v190 op_sel_hi:[0,0,0]
	v_mfma_scale_f32_16x16x128_f8f6f4 v[142:145], v[2:9], v[220:227], v[142:145], v190, v190 op_sel_hi:[0,0,0]
	v_mfma_scale_f32_16x16x128_f8f6f4 v[138:141], v[10:17], v[220:227], v[138:141], v190, v190 op_sel_hi:[0,0,0]
	v_mfma_scale_f32_16x16x128_f8f6f4 v[126:129], v[2:9], v[228:235], v[126:129], v190, v190 op_sel_hi:[0,0,0]
	v_mfma_scale_f32_16x16x128_f8f6f4 v[122:125], v[10:17], v[228:235], v[122:125], v190, v190 op_sel_hi:[0,0,0]
	v_mfma_scale_f32_16x16x128_f8f6f4 v[110:113], v[2:9], v[236:243], v[110:113], v190, v190 op_sel_hi:[0,0,0]
	v_mfma_scale_f32_16x16x128_f8f6f4 v[106:109], v[10:17], v[236:243], v[106:109], v190, v190 op_sel_hi:[0,0,0]
	s_setprio 0
	s_setprio 1
	v_mfma_scale_f32_16x16x128_f8f6f4 v[150:153], v[18:25], v[212:219], v[150:153], v190, v190 op_sel_hi:[0,0,0]
	v_mfma_scale_f32_16x16x128_f8f6f4 v[146:149], v[26:33], v[212:219], v[146:149], v190, v190 op_sel_hi:[0,0,0]
	v_mfma_scale_f32_16x16x128_f8f6f4 v[134:137], v[18:25], v[220:227], v[134:137], v190, v190 op_sel_hi:[0,0,0]
	v_mfma_scale_f32_16x16x128_f8f6f4 v[130:133], v[26:33], v[220:227], v[130:133], v190, v190 op_sel_hi:[0,0,0]
	v_mfma_scale_f32_16x16x128_f8f6f4 v[118:121], v[18:25], v[228:235], v[118:121], v190, v190 op_sel_hi:[0,0,0]
	v_mfma_scale_f32_16x16x128_f8f6f4 v[114:117], v[26:33], v[228:235], v[114:117], v190, v190 op_sel_hi:[0,0,0]
	v_mfma_scale_f32_16x16x128_f8f6f4 v[102:105], v[18:25], v[236:243], v[102:105], v190, v190 op_sel_hi:[0,0,0]
	v_mfma_scale_f32_16x16x128_f8f6f4 v[98:101], v[26:33], v[236:243], v[98:101], v190, v190 op_sel_hi:[0,0,0]
	s_setprio 0
	s_barrier
	s_add_i32 s62, s84, s65
	v_lshl_add_u64 v[182:183], v[182:183], 0, s[20:21]
	s_mov_b32 m0, s62
	ds_read_b128 v[212:215], v208 offset:49152
	ds_read_b128 v[216:219], v208 offset:50176
	ds_read_b128 v[220:223], v208 offset:51200
	ds_read_b128 v[224:227], v208 offset:52224
	ds_read_b128 v[228:231], v208 offset:53248
	ds_read_b128 v[232:235], v208 offset:54272
	ds_read_b128 v[236:239], v208 offset:55296
	ds_read_b128 v[240:243], v208 offset:56320
	global_load_lds_dwordx4 v[182:183], off
	s_add_i32 m0, s62, 0x2000
	s_add_u32 s48, s48, 0x10080
	v_lshl_add_u64 v[182:183], v[184:185], 0, s[20:21]
	s_addc_u32 s49, s49, 0
	s_add_i32 s62, s85, s65
	global_load_lds_dwordx4 v[182:183], off
	v_lshl_add_u64 v[182:183], s[48:49], 0, v[162:163]
	s_mov_b32 m0, s62
	s_nop 0
	global_load_lds_dwordx4 v[182:183], off
	v_lshl_add_u64 v[182:183], s[48:49], 0, v[168:169]
	s_add_i32 m0, s62, 0x2000
	s_nop 0
	global_load_lds_dwordx4 v[182:183], off
	v_lshl_add_u64 v[182:183], v[186:187], 0, s[20:21]
	s_mov_b32 m0, s72
	s_nop 0
	global_load_lds_dwordx4 v[182:183], off
	v_lshl_add_u64 v[182:183], v[188:189], 0, s[20:21]
	s_mov_b32 m0, s73
	s_nop 0
	global_load_lds_dwordx4 v[182:183], off
	s_waitcnt vmcnt(8)
	s_waitcnt lgkmcnt(0)
	s_barrier
	s_setprio 1
	v_mfma_scale_f32_16x16x128_f8f6f4 v[94:97], v[2:9], v[212:219], v[94:97], v190, v190 op_sel_hi:[0,0,0]
	v_mfma_scale_f32_16x16x128_f8f6f4 v[90:93], v[10:17], v[212:219], v[90:93], v190, v190 op_sel_hi:[0,0,0]
	v_mfma_scale_f32_16x16x128_f8f6f4 v[78:81], v[2:9], v[220:227], v[78:81], v190, v190 op_sel_hi:[0,0,0]
	v_mfma_scale_f32_16x16x128_f8f6f4 v[74:77], v[10:17], v[220:227], v[74:77], v190, v190 op_sel_hi:[0,0,0]
	v_mfma_scale_f32_16x16x128_f8f6f4 v[62:65], v[2:9], v[228:235], v[62:65], v190, v190 op_sel_hi:[0,0,0]
	v_mfma_scale_f32_16x16x128_f8f6f4 v[58:61], v[10:17], v[228:235], v[58:61], v190, v190 op_sel_hi:[0,0,0]
	v_mfma_scale_f32_16x16x128_f8f6f4 v[46:49], v[2:9], v[236:243], v[46:49], v190, v190 op_sel_hi:[0,0,0]
	v_mfma_scale_f32_16x16x128_f8f6f4 v[42:45], v[10:17], v[236:243], v[42:45], v190, v190 op_sel_hi:[0,0,0]
	s_setprio 0
	s_setprio 1
	v_mfma_scale_f32_16x16x128_f8f6f4 v[86:89], v[18:25], v[212:219], v[86:89], v190, v190 op_sel_hi:[0,0,0]
	v_mfma_scale_f32_16x16x128_f8f6f4 v[82:85], v[26:33], v[212:219], v[82:85], v190, v190 op_sel_hi:[0,0,0]
	v_mfma_scale_f32_16x16x128_f8f6f4 v[70:73], v[18:25], v[220:227], v[70:73], v190, v190 op_sel_hi:[0,0,0]
	v_mfma_scale_f32_16x16x128_f8f6f4 v[66:69], v[26:33], v[220:227], v[66:69], v190, v190 op_sel_hi:[0,0,0]
	v_mfma_scale_f32_16x16x128_f8f6f4 v[54:57], v[18:25], v[228:235], v[54:57], v190, v190 op_sel_hi:[0,0,0]
	v_mfma_scale_f32_16x16x128_f8f6f4 v[50:53], v[26:33], v[228:235], v[50:53], v190, v190 op_sel_hi:[0,0,0]
	v_mfma_scale_f32_16x16x128_f8f6f4 v[38:41], v[18:25], v[236:243], v[38:41], v190, v190 op_sel_hi:[0,0,0]
	v_mfma_scale_f32_16x16x128_f8f6f4 v[34:37], v[26:33], v[236:243], v[34:37], v190, v190 op_sel_hi:[0,0,0]
	s_setprio 0
	s_barrier
	s_add_i32 s97, s97, 2
	s_add_u32 s46, s46, 0x100
	s_addc_u32 s47, s47, 0
	s_add_u32 s95, s95, 0x100
	s_addc_u32 s96, s96, 0
	s_cmp_gt_u32 s97, 13
	s_cbranch_scc0 .LBB0_346
	s_and_b64 vcc, exec, s[24:25]
	s_cbranch_vccz .LBB0_349
	s_barrier

; #define PG8_STAGE(bufoff, gbase, voff) do { _Pragma("unroll") for (int _i = 0; _i < 2; ++_i) \
;         __builtin_amdgcn_global_load_lds((const unsigned*)((const char*)(gbase) + (voff)[_i]), (LAS unsigned*)(lds + (bufoff) + ldsw + _i * 8192), 16, 0, 0); } while (0)
; #define PG8_LDA(dst, b, h) do { _Pragma("unroll") for (int m = 0; m < 4; ++m) { if constexpr (F8) dst##8[m] = PG8_LD32(lds + PG8_SA(b, h) + aoff + m * 2048); \
;         else { _Pragma("unroll") for (int k = 0; k < 2; ++k) dst[m][k] = *(const LAS bf16x8*)(lds + PG8_SA(b, h) + aoff + m * 2048 + k * 1024); } } } while (0)
; #define PG8_LDB(dst, b, h) do { _Pragma("unroll") for (int n = 0; n < 2; ++n) { if constexpr (F8) dst##8[n] = PG8_LD32(lds + PG8_SB(b, h) + boff + n * 2048); \
;         else { _Pragma("unroll") for (int k = 0; k < 2; ++k) dst[n][k] = *(const LAS bf16x8*)(lds + PG8_SB(b, h) + boff + n * 2048 + k * 1024); } } } while (0)
; #define PG8_WAIT_V(n) asm volatile("s_waitcnt vmcnt(" #n ")" ::: "memory")
; #define PG8_WAIT_L(n) asm volatile("s_waitcnt lgkmcnt(" #n ")" ::: "memory")
; #define PG8_BAR __builtin_amdgcn_s_barrier()
; #define PG8_SCHED __builtin_amdgcn_sched_barrier(0)
; template <class Epi, class Sched, bool GATHER, bool F8 = false>
; __device__ __forceinline__ void gemm_phase(LAS unsigned char* lds, const int K, const Sched& S, const Epi& E) {
;     ...
;             PG8_LDB(B0, 0, 0); PG8_LDB(B1, 0, 1); PG8_SCHED; PG8_LDA(At, 0, 0); PG8_STAGE(PG8_SA(1, 1), a1, vA[1]);
;             PG8_WAIT_V(8); PG8_WAIT_L(0); PG8_BAR; PG8_MMA(0, 0, At, B0); PG8_MMA(0, 1, At, B1); PG8_BAR; PG8_SCHED;
;             PG8_LDA(At, 0, 1); PG8_STAGE(PG8_SB(0, 0), b2, voffB); PG8_STAGE(PG8_SB(0, 1), b2 + hstepB, voffB); PG8_STAGE(PG8_SA(0, 0), a2, vN[0]);
;             PG8_WAIT_V(8); PG8_WAIT_L(0); PG8_BAR; PG8_MMA(1, 0, At, B0); PG8_MMA(1, 1, At, B1); PG8_BAR; PG8_SCHED;
.LBB0_558:
	v_add_u32_e32 v156, s74, v165
	ds_read_b128 v[2:5], v156
	ds_read_b128 v[6:9], v156 offset:1024
	ds_read_b128 v[182:185], v156 offset:2048
	ds_read_b128 v[186:189], v156 offset:3072
	v_add_u32_e32 v156, s75, v165
	ds_read_b128 v[190:193], v156
	ds_read_b128 v[194:197], v156 offset:1024
	ds_read_b128 v[198:201], v156 offset:2048
	ds_read_b128 v[202:205], v156 offset:3072
	s_add_u32 s60, s4, 0x80
	s_addc_u32 s61, s5, 0
	s_cmp_eq_u32 s55, 4
	s_cselect_b32 s63, s57, s61
	s_cselect_b32 s62, s56, s60
	s_cselect_b32 s61, s53, s7
	s_cselect_b32 s60, s52, s6
	v_lshl_add_u64 v[230:231], s[4:5], 0, v[152:153]
	s_add_i32 m0, s66, 0xc000
	ds_read_b128 v[156:159], v179
	ds_read_b128 v[160:163], v179 offset:1024
	ds_read_b128 v[206:209], v179 offset:2048
	ds_read_b128 v[210:213], v179 offset:3072
	ds_read_b128 v[214:217], v179 offset:4096
	ds_read_b128 v[218:221], v179 offset:5120
	ds_read_b128 v[222:225], v179 offset:6144
	ds_read_b128 v[226:229], v179 offset:7168
	global_load_lds_dwordx4 v[230:231], off
	v_lshl_add_u64 v[230:231], s[4:5], 0, v[154:155]
	s_add_i32 m0, s66, 0xe000
	s_nop 0
	global_load_lds_dwordx4 v[230:231], off
	s_waitcnt vmcnt(8)
	s_waitcnt lgkmcnt(0)
	s_barrier
	s_setprio 1
	v_mfma_scale_f32_16x16x128_f8f6f4 v[134:137], v[2:9], v[156:163], v[134:137], v1, v1 op_sel_hi:[0,0,0]
	v_mfma_scale_f32_16x16x128_f8f6f4 v[130:133], v[182:189], v[156:163], v[130:133], v1, v1 op_sel_hi:[0,0,0]
	v_mfma_scale_f32_16x16x128_f8f6f4 v[126:129], v[2:9], v[206:213], v[126:129], v1, v1 op_sel_hi:[0,0,0]
	v_mfma_scale_f32_16x16x128_f8f6f4 v[122:125], v[182:189], v[206:213], v[122:125], v1, v1 op_sel_hi:[0,0,0]
	v_mfma_scale_f32_16x16x128_f8f6f4 v[118:121], v[2:9], v[214:221], v[118:121], v1, v1 op_sel_hi:[0,0,0]
	v_mfma_scale_f32_16x16x128_f8f6f4 v[114:117], v[182:189], v[214:221], v[114:117], v1, v1 op_sel_hi:[0,0,0]
	v_mfma_scale_f32_16x16x128_f8f6f4 v[110:113], v[2:9], v[222:229], v[110:113], v1, v1 op_sel_hi:[0,0,0]
	v_mfma_scale_f32_16x16x128_f8f6f4 v[106:109], v[182:189], v[222:229], v[106:109], v1, v1 op_sel_hi:[0,0,0]
	s_setprio 0
	s_setprio 1
	v_mfma_scale_f32_16x16x128_f8f6f4 v[102:105], v[190:197], v[156:163], v[102:105], v1, v1 op_sel_hi:[0,0,0]
	v_mfma_scale_f32_16x16x128_f8f6f4 v[98:101], v[198:205], v[156:163], v[98:101], v1, v1 op_sel_hi:[0,0,0]
	v_mfma_scale_f32_16x16x128_f8f6f4 v[94:97], v[190:197], v[206:213], v[94:97], v1, v1 op_sel_hi:[0,0,0]
	v_mfma_scale_f32_16x16x128_f8f6f4 v[90:93], v[198:205], v[206:213], v[90:93], v1, v1 op_sel_hi:[0,0,0]
	v_mfma_scale_f32_16x16x128_f8f6f4 v[86:89], v[190:197], v[214:221], v[86:89], v1, v1 op_sel_hi:[0,0,0]
	v_mfma_scale_f32_16x16x128_f8f6f4 v[82:85], v[198:205], v[214:221], v[82:85], v1, v1 op_sel_hi:[0,0,0]
	v_mfma_scale_f32_16x16x128_f8f6f4 v[78:81], v[190:197], v[222:229], v[78:81], v1, v1 op_sel_hi:[0,0,0]
	v_mfma_scale_f32_16x16x128_f8f6f4 v[74:77], v[198:205], v[222:229], v[74:77], v1, v1 op_sel_hi:[0,0,0]
	s_setprio 0
	s_barrier
	s_add_i32 s77, s74, s65
	v_lshl_add_u64 v[156:157], s[60:61], 0, v[138:139]
	s_mov_b32 m0, s77
	ds_read_b128 v[206:209], v179 offset:16384
	ds_read_b128 v[210:213], v179 offset:17408
	ds_read_b128 v[214:217], v179 offset:18432
	ds_read_b128 v[218:221], v179 offset:19456
	ds_read_b128 v[222:225], v179 offset:20480
	ds_read_b128 v[226:229], v179 offset:21504
	ds_read_b128 v[230:233], v179 offset:22528
	ds_read_b128 v[234:237], v179 offset:23552
	global_load_lds_dwordx4 v[156:157], off
	s_add_i32 m0, s77, 0x2000
	s_add_u32 s78, s60, 0x8000
	v_lshl_add_u64 v[158:159], s[60:61], 0, v[144:145]
	s_addc_u32 s79, s61, 0
	s_add_i32 s77, s75, s65
	global_load_lds_dwordx4 v[158:159], off
	v_lshl_add_u64 v[160:161], s[78:79], 0, v[138:139]
	s_mov_b32 m0, s77
	v_lshl_add_u64 v[162:163], s[62:63], 0, v[146:147]
	global_load_lds_dwordx4 v[160:161], off
	v_lshl_add_u64 v[160:161], s[78:79], 0, v[144:145]
	s_add_i32 m0, s77, 0x2000
	s_nop 0
	global_load_lds_dwordx4 v[160:161], off
	v_lshl_add_u64 v[160:161], s[62:63], 0, v[140:141]
	s_mov_b32 m0, s66
	s_nop 0
	global_load_lds_dwordx4 v[160:161], off
	s_mov_b32 m0, s67
	s_nop 0
	global_load_lds_dwordx4 v[162:163], off
	s_waitcnt vmcnt(8)
	s_waitcnt lgkmcnt(0)
	s_barrier
	s_setprio 1
	v_mfma_scale_f32_16x16x128_f8f6f4 v[70:73], v[2:9], v[206:213], v[70:73], v1, v1 op_sel_hi:[0,0,0]
	v_mfma_scale_f32_16x16x128_f8f6f4 v[66:69], v[182:189], v[206:213], v[66:69], v1, v1 op_sel_hi:[0,0,0]
	v_mfma_scale_f32_16x16x128_f8f6f4 v[62:65], v[2:9], v[214:221], v[62:65], v1, v1 op_sel_hi:[0,0,0]
	v_mfma_scale_f32_16x16x128_f8f6f4 v[58:61], v[182:189], v[214:221], v[58:61], v1, v1 op_sel_hi:[0,0,0]
	v_mfma_scale_f32_16x16x128_f8f6f4 v[54:57], v[2:9], v[222:229], v[54:57], v1, v1 op_sel_hi:[0,0,0]
	v_mfma_scale_f32_16x16x128_f8f6f4 v[50:53], v[182:189], v[222:229], v[50:53], v1, v1 op_sel_hi:[0,0,0]
	v_mfma_scale_f32_16x16x128_f8f6f4 v[46:49], v[2:9], v[230:237], v[46:49], v1, v1 op_sel_hi:[0,0,0]
	v_mfma_scale_f32_16x16x128_f8f6f4 v[42:45], v[182:189], v[230:237], v[42:45], v1, v1 op_sel_hi:[0,0,0]
	s_setprio 0
	s_setprio 1
	v_mfma_scale_f32_16x16x128_f8f6f4 v[38:41], v[190:197], v[206:213], v[38:41], v1, v1 op_sel_hi:[0,0,0]
	v_mfma_scale_f32_16x16x128_f8f6f4 v[34:37], v[198:205], v[206:213], v[34:37], v1, v1 op_sel_hi:[0,0,0]
	v_mfma_scale_f32_16x16x128_f8f6f4 v[30:33], v[190:197], v[214:221], v[30:33], v1, v1 op_sel_hi:[0,0,0]
	v_mfma_scale_f32_16x16x128_f8f6f4 v[26:29], v[198:205], v[214:221], v[26:29], v1, v1 op_sel_hi:[0,0,0]
	v_mfma_scale_f32_16x16x128_f8f6f4 v[22:25], v[190:197], v[222:229], v[22:25], v1, v1 op_sel_hi:[0,0,0]
	v_mfma_scale_f32_16x16x128_f8f6f4 v[18:21], v[198:205], v[222:229], v[18:21], v1, v1 op_sel_hi:[0,0,0]
	v_mfma_scale_f32_16x16x128_f8f6f4 v[14:17], v[190:197], v[230:237], v[14:17], v1, v1 op_sel_hi:[0,0,0]
	v_mfma_scale_f32_16x16x128_f8f6f4 v[10:13], v[198:205], v[230:237], v[10:13], v1, v1 op_sel_hi:[0,0,0]
	s_setprio 0
	s_barrier
; #define PG8_STAGE(bufoff, gbase, voff) do { _Pragma("unroll") for (int _i = 0; _i < 2; ++_i) \
;         __builtin_amdgcn_global_load_lds((const unsigned*)((const char*)(gbase) + (voff)[_i]), (LAS unsigned*)(lds + (bufoff) + ldsw + _i * 8192), 16, 0, 0); } while (0)
; #define PG8_LDA(dst, b, h) do { _Pragma("unroll") for (int m = 0; m < 4; ++m) { if constexpr (F8) dst##8[m] = PG8_LD32(lds + PG8_SA(b, h) + aoff + m * 2048); \
;         else { _Pragma("unroll") for (int k = 0; k < 2; ++k) dst[m][k] = *(const LAS bf16x8*)(lds + PG8_SA(b, h) + aoff + m * 2048 + k * 1024); } } } while (0)
; #define PG8_LDB(dst, b, h) do { _Pragma("unroll") for (int n = 0; n < 2; ++n) { if constexpr (F8) dst##8[n] = PG8_LD32(lds + PG8_SB(b, h) + boff + n * 2048); \
;         else { _Pragma("unroll") for (int k = 0; k < 2; ++k) dst[n][k] = *(const LAS bf16x8*)(lds + PG8_SB(b, h) + boff + n * 2048 + k * 1024); } } } while (0)
; #define PG8_WAIT_V(n) asm volatile("s_waitcnt vmcnt(" #n ")" ::: "memory")
; #define PG8_WAIT_L(n) asm volatile("s_waitcnt lgkmcnt(" #n ")" ::: "memory")
; #define PG8_BAR __builtin_amdgcn_s_barrier()
; #define PG8_SCHED __builtin_amdgcn_sched_barrier(0)
; template <class Epi, class Sched, bool GATHER, bool F8 = false>
; __device__ __forceinline__ void gemm_phase(LAS unsigned char* lds, const int K, const Sched& S, const Epi& E) {
;     ...
;             PG8_LDB(B0, 1, 0); PG8_LDB(B1, 1, 1); PG8_SCHED; PG8_LDA(At, 1, 0); PG8_STAGE(PG8_SA(0, 1), a2, vN[1]);
;             PG8_WAIT_V(8); PG8_WAIT_L(0); PG8_BAR; PG8_MMA(0, 0, At, B0); PG8_MMA(0, 1, At, B1); PG8_BAR; PG8_SCHED;
;             PG8_LDA(At, 1, 1); PG8_STAGE(PG8_SB(1, 0), b3, voffB); PG8_STAGE(PG8_SB(1, 1), b3 + hstepB, voffB); PG8_STAGE(PG8_SA(1, 0), a3, vN[0]);
;             PG8_WAIT_V(8); PG8_WAIT_L(0); PG8_BAR; PG8_MMA(1, 0, At, B0); PG8_MMA(1, 1, At, B1); PG8_BAR; PG8_SCHED;
;         }
;         if (wr == 0) PG8_BAR;
	s_add_i32 s77, 0, 0x18000
	s_add_i32 s78, 0, 0x1c000
	v_add_u32_e32 v2, s77, v165
	v_add_u32_e32 v181, s78, v165
	ds_read_b128 v[182:185], v2
	ds_read_b128 v[186:189], v2 offset:1024
	ds_read_b128 v[190:193], v2 offset:2048
	ds_read_b128 v[194:197], v2 offset:3072
	ds_read_b128 v[2:5], v181
	ds_read_b128 v[6:9], v181 offset:1024
	ds_read_b128 v[198:201], v181 offset:2048
	ds_read_b128 v[202:205], v181 offset:3072
	s_mov_b32 m0, s68
	v_lshl_add_u64 v[238:239], s[62:63], 0, v[142:143]
	ds_read_b128 v[206:209], v179 offset:32768
	ds_read_b128 v[210:213], v179 offset:33792
	ds_read_b128 v[214:217], v179 offset:34816
	ds_read_b128 v[218:221], v179 offset:35840
	ds_read_b128 v[222:225], v179 offset:36864
	ds_read_b128 v[226:229], v179 offset:37888
	ds_read_b128 v[230:233], v179 offset:38912
	ds_read_b128 v[234:237], v179 offset:39936
	global_load_lds_dwordx4 v[238:239], off
	v_lshl_add_u64 v[238:239], s[62:63], 0, v[148:149]
	s_mov_b32 m0, s69
	s_nop 0
	global_load_lds_dwordx4 v[238:239], off
	s_waitcnt vmcnt(8)
	s_waitcnt lgkmcnt(0)
	s_barrier
	s_setprio 1
	v_mfma_scale_f32_16x16x128_f8f6f4 v[134:137], v[182:189], v[206:213], v[134:137], v1, v1 op_sel_hi:[0,0,0]
	v_mfma_scale_f32_16x16x128_f8f6f4 v[130:133], v[190:197], v[206:213], v[130:133], v1, v1 op_sel_hi:[0,0,0]
	v_mfma_scale_f32_16x16x128_f8f6f4 v[126:129], v[182:189], v[214:221], v[126:129], v1, v1 op_sel_hi:[0,0,0]
	v_mfma_scale_f32_16x16x128_f8f6f4 v[122:125], v[190:197], v[214:221], v[122:125], v1, v1 op_sel_hi:[0,0,0]
	v_mfma_scale_f32_16x16x128_f8f6f4 v[118:121], v[182:189], v[222:229], v[118:121], v1, v1 op_sel_hi:[0,0,0]
	v_mfma_scale_f32_16x16x128_f8f6f4 v[114:117], v[190:197], v[222:229], v[114:117], v1, v1 op_sel_hi:[0,0,0]
	v_mfma_scale_f32_16x16x128_f8f6f4 v[110:113], v[182:189], v[230:237], v[110:113], v1, v1 op_sel_hi:[0,0,0]
	v_mfma_scale_f32_16x16x128_f8f6f4 v[106:109], v[190:197], v[230:237], v[106:109], v1, v1 op_sel_hi:[0,0,0]
	s_setprio 0
	s_setprio 1
	v_mfma_scale_f32_16x16x128_f8f6f4 v[102:105], v[2:9], v[206:213], v[102:105], v1, v1 op_sel_hi:[0,0,0]
	v_mfma_scale_f32_16x16x128_f8f6f4 v[98:101], v[198:205], v[206:213], v[98:101], v1, v1 op_sel_hi:[0,0,0]
	v_mfma_scale_f32_16x16x128_f8f6f4 v[94:97], v[2:9], v[214:221], v[94:97], v1, v1 op_sel_hi:[0,0,0]
	v_mfma_scale_f32_16x16x128_f8f6f4 v[90:93], v[198:205], v[214:221], v[90:93], v1, v1 op_sel_hi:[0,0,0]
	v_mfma_scale_f32_16x16x128_f8f6f4 v[86:89], v[2:9], v[222:229], v[86:89], v1, v1 op_sel_hi:[0,0,0]
	v_mfma_scale_f32_16x16x128_f8f6f4 v[82:85], v[198:205], v[222:229], v[82:85], v1, v1 op_sel_hi:[0,0,0]
	v_mfma_scale_f32_16x16x128_f8f6f4 v[78:81], v[2:9], v[230:237], v[78:81], v1, v1 op_sel_hi:[0,0,0]
	v_mfma_scale_f32_16x16x128_f8f6f4 v[74:77], v[198:205], v[230:237], v[74:77], v1, v1 op_sel_hi:[0,0,0]
	s_setprio 0
	s_barrier
	s_add_i32 s62, s77, s65
	v_lshl_add_u64 v[156:157], v[156:157], 0, s[42:43]
	s_mov_b32 m0, s62
	ds_read_b128 v[206:209], v179 offset:49152
	ds_read_b128 v[210:213], v179 offset:50176
	ds_read_b128 v[214:217], v179 offset:51200
	ds_read_b128 v[218:221], v179 offset:52224
	ds_read_b128 v[222:225], v179 offset:53248
	ds_read_b128 v[226:229], v179 offset:54272
	ds_read_b128 v[230:233], v179 offset:55296
	ds_read_b128 v[234:237], v179 offset:56320
	global_load_lds_dwordx4 v[156:157], off
	s_add_i32 m0, s62, 0x2000
	s_add_u32 s60, s60, 0x8080
	v_lshl_add_u64 v[156:157], v[158:159], 0, s[42:43]
	s_addc_u32 s61, s61, 0
	s_add_i32 s62, s78, s65
	global_load_lds_dwordx4 v[156:157], off
	v_lshl_add_u64 v[156:157], s[60:61], 0, v[138:139]
	s_mov_b32 m0, s62
	s_nop 0
	global_load_lds_dwordx4 v[156:157], off
	v_lshl_add_u64 v[156:157], s[60:61], 0, v[144:145]
	s_add_i32 m0, s62, 0x2000
	s_nop 0
	global_load_lds_dwordx4 v[156:157], off
	v_lshl_add_u64 v[156:157], v[160:161], 0, s[42:43]
	s_mov_b32 m0, s70
	s_nop 0
	global_load_lds_dwordx4 v[156:157], off
	v_lshl_add_u64 v[156:157], v[162:163], 0, s[42:43]
	s_mov_b32 m0, s71
	s_nop 0
	global_load_lds_dwordx4 v[156:157], off
	s_waitcnt vmcnt(8)
	s_waitcnt lgkmcnt(0)
	s_barrier
	s_setprio 1
	v_mfma_scale_f32_16x16x128_f8f6f4 v[70:73], v[182:189], v[206:213], v[70:73], v1, v1 op_sel_hi:[0,0,0]
	v_mfma_scale_f32_16x16x128_f8f6f4 v[66:69], v[190:197], v[206:213], v[66:69], v1, v1 op_sel_hi:[0,0,0]
	v_mfma_scale_f32_16x16x128_f8f6f4 v[62:65], v[182:189], v[214:221], v[62:65], v1, v1 op_sel_hi:[0,0,0]
	v_mfma_scale_f32_16x16x128_f8f6f4 v[58:61], v[190:197], v[214:221], v[58:61], v1, v1 op_sel_hi:[0,0,0]
	v_mfma_scale_f32_16x16x128_f8f6f4 v[54:57], v[182:189], v[222:229], v[54:57], v1, v1 op_sel_hi:[0,0,0]
	v_mfma_scale_f32_16x16x128_f8f6f4 v[50:53], v[190:197], v[222:229], v[50:53], v1, v1 op_sel_hi:[0,0,0]
	v_mfma_scale_f32_16x16x128_f8f6f4 v[46:49], v[182:189], v[230:237], v[46:49], v1, v1 op_sel_hi:[0,0,0]
	v_mfma_scale_f32_16x16x128_f8f6f4 v[42:45], v[190:197], v[230:237], v[42:45], v1, v1 op_sel_hi:[0,0,0]
	s_setprio 0
	s_setprio 1
	v_mfma_scale_f32_16x16x128_f8f6f4 v[38:41], v[2:9], v[206:213], v[38:41], v1, v1 op_sel_hi:[0,0,0]
	v_mfma_scale_f32_16x16x128_f8f6f4 v[34:37], v[198:205], v[206:213], v[34:37], v1, v1 op_sel_hi:[0,0,0]
	v_mfma_scale_f32_16x16x128_f8f6f4 v[30:33], v[2:9], v[214:221], v[30:33], v1, v1 op_sel_hi:[0,0,0]
	v_mfma_scale_f32_16x16x128_f8f6f4 v[26:29], v[198:205], v[214:221], v[26:29], v1, v1 op_sel_hi:[0,0,0]
	v_mfma_scale_f32_16x16x128_f8f6f4 v[22:25], v[2:9], v[222:229], v[22:25], v1, v1 op_sel_hi:[0,0,0]
	v_mfma_scale_f32_16x16x128_f8f6f4 v[18:21], v[198:205], v[222:229], v[18:21], v1, v1 op_sel_hi:[0,0,0]
	v_mfma_scale_f32_16x16x128_f8f6f4 v[14:17], v[2:9], v[230:237], v[14:17], v1, v1 op_sel_hi:[0,0,0]
	v_mfma_scale_f32_16x16x128_f8f6f4 v[10:13], v[198:205], v[230:237], v[10:13], v1, v1 op_sel_hi:[0,0,0]
	s_setprio 0
	s_barrier
	s_add_i32 s55, s55, 2
	s_add_u32 s4, s4, 0x100
	s_addc_u32 s5, s5, 0
	s_add_u32 s6, s6, 0x100
	s_addc_u32 s7, s7, 0
	s_cmp_gt_u32 s55, 5
	s_cbranch_scc0 .LBB0_558
	s_and_b64 vcc, exec, s[44:45]
	s_cbranch_vccz .LBB0_561
	s_barrier

; #define PG8_STAGE(bufoff, gbase, voff) do { _Pragma("unroll") for (int _i = 0; _i < 2; ++_i) \
;         __builtin_amdgcn_global_load_lds((const unsigned*)((const char*)(gbase) + (voff)[_i]), (LAS unsigned*)(lds + (bufoff) + ldsw + _i * 8192), 16, 0, 0); } while (0)
; #define PG8_LDA(dst, b, h) do { _Pragma("unroll") for (int m = 0; m < 4; ++m) { if constexpr (F8) dst##8[m] = PG8_LD32(lds + PG8_SA(b, h) + aoff + m * 2048); \
;         else { _Pragma("unroll") for (int k = 0; k < 2; ++k) dst[m][k] = *(const LAS bf16x8*)(lds + PG8_SA(b, h) + aoff + m * 2048 + k * 1024); } } } while (0)
; #define PG8_LDB(dst, b, h) do { _Pragma("unroll") for (int n = 0; n < 2; ++n) { if constexpr (F8) dst##8[n] = PG8_LD32(lds + PG8_SB(b, h) + boff + n * 2048); \
;         else { _Pragma("unroll") for (int k = 0; k < 2; ++k) dst[n][k] = *(const LAS bf16x8*)(lds + PG8_SB(b, h) + boff + n * 2048 + k * 1024); } } } while (0)
; #define PG8_WAIT_V(n) asm volatile("s_waitcnt vmcnt(" #n ")" ::: "memory")
; #define PG8_WAIT_L(n) asm volatile("s_waitcnt lgkmcnt(" #n ")" ::: "memory")
; #define PG8_BAR __builtin_amdgcn_s_barrier()
; #define PG8_SCHED __builtin_amdgcn_sched_barrier(0)
; template <class Epi, class Sched, bool GATHER, bool F8 = false>
; __device__ __forceinline__ void gemm_phase(LAS unsigned char* lds, const int K, const Sched& S, const Epi& E) {
;     ...
;             PG8_LDB(B0, 0, 0); PG8_LDB(B1, 0, 1); PG8_SCHED; PG8_LDA(At, 0, 0); PG8_STAGE(PG8_SA(1, 1), a1, vA[1]);
;             PG8_WAIT_V(8); PG8_WAIT_L(0); PG8_BAR; PG8_MMA(0, 0, At, B0); PG8_MMA(0, 1, At, B1); PG8_BAR; PG8_SCHED;
;             PG8_LDA(At, 0, 1); PG8_STAGE(PG8_SB(0, 0), b2, voffB); PG8_STAGE(PG8_SB(0, 1), b2 + hstepB, voffB); PG8_STAGE(PG8_SA(0, 0), a2, vN[0]);
;             PG8_WAIT_V(8); PG8_WAIT_L(0); PG8_BAR; PG8_MMA(1, 0, At, B0); PG8_MMA(1, 1, At, B1); PG8_BAR; PG8_SCHED;
.LBB0_702:
	ds_read_b128 v[18:21], v191
	ds_read_b128 v[22:25], v191 offset:1024
	ds_read_b128 v[26:29], v191 offset:2048
	ds_read_b128 v[30:33], v191 offset:3072
	ds_read_b128 v[2:5], v192
	ds_read_b128 v[6:9], v192 offset:1024
	ds_read_b128 v[10:13], v192 offset:2048
	ds_read_b128 v[14:17], v192 offset:3072
	s_add_u32 s42, s38, s40
	s_addc_u32 s43, s39, s41
	s_add_u32 s42, s42, 0x2f200100
	s_addc_u32 s43, s43, 0
	s_add_u32 s63, s50, s40
	s_addc_u32 s64, s51, s41
	s_cmpk_eq_i32 s40, 0x700
	s_cselect_b32 s45, s17, s43
	s_cselect_b32 s44, s16, s42
	s_cselect_b32 s43, s21, s64
	s_cselect_b32 s42, s20, s63
	s_mov_b32 m0, s53
	v_lshl_add_u64 v[220:221], v[176:177], 0, s[40:41]
	ds_read_b128 v[180:183], v193
	ds_read_b128 v[184:187], v193 offset:1024
	ds_read_b128 v[196:199], v193 offset:2048
	ds_read_b128 v[200:203], v193 offset:3072
	ds_read_b128 v[204:207], v193 offset:4096
	ds_read_b128 v[208:211], v193 offset:5120
	ds_read_b128 v[212:215], v193 offset:6144
	ds_read_b128 v[216:219], v193 offset:7168
	global_load_lds_dwordx4 v[220:221], off
	v_lshl_add_u64 v[220:221], v[178:179], 0, s[40:41]
	s_mov_b32 m0, s54
	s_nop 0
	global_load_lds_dwordx4 v[220:221], off
	s_waitcnt vmcnt(8)
	s_waitcnt lgkmcnt(0)
	s_barrier
	s_setprio 1
	v_mfma_scale_f32_16x16x128_f8f6f4 v[158:161], v[18:25], v[180:187], v[158:161], v188, v188 op_sel_hi:[0,0,0]
	v_mfma_scale_f32_16x16x128_f8f6f4 v[154:157], v[26:33], v[180:187], v[154:157], v188, v188 op_sel_hi:[0,0,0]
	v_mfma_scale_f32_16x16x128_f8f6f4 v[142:145], v[18:25], v[196:203], v[142:145], v188, v188 op_sel_hi:[0,0,0]
	v_mfma_scale_f32_16x16x128_f8f6f4 v[138:141], v[26:33], v[196:203], v[138:141], v188, v188 op_sel_hi:[0,0,0]
	v_mfma_scale_f32_16x16x128_f8f6f4 v[126:129], v[18:25], v[204:211], v[126:129], v188, v188 op_sel_hi:[0,0,0]
	v_mfma_scale_f32_16x16x128_f8f6f4 v[122:125], v[26:33], v[204:211], v[122:125], v188, v188 op_sel_hi:[0,0,0]
	v_mfma_scale_f32_16x16x128_f8f6f4 v[110:113], v[18:25], v[212:219], v[110:113], v188, v188 op_sel_hi:[0,0,0]
	v_mfma_scale_f32_16x16x128_f8f6f4 v[106:109], v[26:33], v[212:219], v[106:109], v188, v188 op_sel_hi:[0,0,0]
	s_setprio 0
	s_setprio 1
	v_mfma_scale_f32_16x16x128_f8f6f4 v[150:153], v[2:9], v[180:187], v[150:153], v188, v188 op_sel_hi:[0,0,0]
	v_mfma_scale_f32_16x16x128_f8f6f4 v[146:149], v[10:17], v[180:187], v[146:149], v188, v188 op_sel_hi:[0,0,0]
	v_mfma_scale_f32_16x16x128_f8f6f4 v[134:137], v[2:9], v[196:203], v[134:137], v188, v188 op_sel_hi:[0,0,0]
	v_mfma_scale_f32_16x16x128_f8f6f4 v[130:133], v[10:17], v[196:203], v[130:133], v188, v188 op_sel_hi:[0,0,0]
	v_mfma_scale_f32_16x16x128_f8f6f4 v[118:121], v[2:9], v[204:211], v[118:121], v188, v188 op_sel_hi:[0,0,0]
	v_mfma_scale_f32_16x16x128_f8f6f4 v[114:117], v[10:17], v[204:211], v[114:117], v188, v188 op_sel_hi:[0,0,0]
	v_mfma_scale_f32_16x16x128_f8f6f4 v[102:105], v[2:9], v[212:219], v[102:105], v188, v188 op_sel_hi:[0,0,0]
	v_mfma_scale_f32_16x16x128_f8f6f4 v[98:101], v[10:17], v[212:219], v[98:101], v188, v188 op_sel_hi:[0,0,0]
	s_setprio 0
	s_barrier
	s_mov_b32 m0, s55
	v_lshl_add_u64 v[180:181], s[42:43], 0, v[162:163]
	s_add_u32 s64, s42, 0x10000
	ds_read_b128 v[196:199], v193 offset:16384
	ds_read_b128 v[200:203], v193 offset:17408
	ds_read_b128 v[204:207], v193 offset:18432
	ds_read_b128 v[208:211], v193 offset:19456
	ds_read_b128 v[212:215], v193 offset:20480
	ds_read_b128 v[216:219], v193 offset:21504
	ds_read_b128 v[220:223], v193 offset:22528
	ds_read_b128 v[224:227], v193 offset:23552
	global_load_lds_dwordx4 v[180:181], off
	v_lshl_add_u64 v[182:183], s[42:43], 0, v[168:169]
	s_mov_b32 m0, s56
	s_addc_u32 s65, s43, 0
	global_load_lds_dwordx4 v[182:183], off
	v_lshl_add_u64 v[184:185], s[64:65], 0, v[162:163]
	s_mov_b32 m0, s57
	v_lshl_add_u64 v[186:187], s[44:45], 0, v[172:173]
	global_load_lds_dwordx4 v[184:185], off
	v_lshl_add_u64 v[184:185], s[64:65], 0, v[168:169]
	s_mov_b32 m0, s58
	s_nop 0
	global_load_lds_dwordx4 v[184:185], off
	v_lshl_add_u64 v[184:185], s[44:45], 0, v[164:165]
	s_mov_b32 m0, s1
	s_nop 0
	global_load_lds_dwordx4 v[184:185], off
	s_mov_b32 m0, s6
	s_nop 0
	global_load_lds_dwordx4 v[186:187], off
	s_waitcnt vmcnt(8)
	s_waitcnt lgkmcnt(0)
	s_barrier
	s_setprio 1
	v_mfma_scale_f32_16x16x128_f8f6f4 v[94:97], v[18:25], v[196:203], v[94:97], v188, v188 op_sel_hi:[0,0,0]
	v_mfma_scale_f32_16x16x128_f8f6f4 v[90:93], v[26:33], v[196:203], v[90:93], v188, v188 op_sel_hi:[0,0,0]
	v_mfma_scale_f32_16x16x128_f8f6f4 v[78:81], v[18:25], v[204:211], v[78:81], v188, v188 op_sel_hi:[0,0,0]
	v_mfma_scale_f32_16x16x128_f8f6f4 v[74:77], v[26:33], v[204:211], v[74:77], v188, v188 op_sel_hi:[0,0,0]
	v_mfma_scale_f32_16x16x128_f8f6f4 v[62:65], v[18:25], v[212:219], v[62:65], v188, v188 op_sel_hi:[0,0,0]
	v_mfma_scale_f32_16x16x128_f8f6f4 v[58:61], v[26:33], v[212:219], v[58:61], v188, v188 op_sel_hi:[0,0,0]
	v_mfma_scale_f32_16x16x128_f8f6f4 v[46:49], v[18:25], v[220:227], v[46:49], v188, v188 op_sel_hi:[0,0,0]
	v_mfma_scale_f32_16x16x128_f8f6f4 v[42:45], v[26:33], v[220:227], v[42:45], v188, v188 op_sel_hi:[0,0,0]
	s_setprio 0
	s_setprio 1
	v_mfma_scale_f32_16x16x128_f8f6f4 v[86:89], v[2:9], v[196:203], v[86:89], v188, v188 op_sel_hi:[0,0,0]
	v_mfma_scale_f32_16x16x128_f8f6f4 v[82:85], v[10:17], v[196:203], v[82:85], v188, v188 op_sel_hi:[0,0,0]
	v_mfma_scale_f32_16x16x128_f8f6f4 v[70:73], v[2:9], v[204:211], v[70:73], v188, v188 op_sel_hi:[0,0,0]
	v_mfma_scale_f32_16x16x128_f8f6f4 v[66:69], v[10:17], v[204:211], v[66:69], v188, v188 op_sel_hi:[0,0,0]
	v_mfma_scale_f32_16x16x128_f8f6f4 v[54:57], v[2:9], v[212:219], v[54:57], v188, v188 op_sel_hi:[0,0,0]
	v_mfma_scale_f32_16x16x128_f8f6f4 v[50:53], v[10:17], v[212:219], v[50:53], v188, v188 op_sel_hi:[0,0,0]
	v_mfma_scale_f32_16x16x128_f8f6f4 v[38:41], v[2:9], v[220:227], v[38:41], v188, v188 op_sel_hi:[0,0,0]
	v_mfma_scale_f32_16x16x128_f8f6f4 v[34:37], v[10:17], v[220:227], v[34:37], v188, v188 op_sel_hi:[0,0,0]
	s_setprio 0
	s_barrier
; #define PG8_STAGE(bufoff, gbase, voff) do { _Pragma("unroll") for (int _i = 0; _i < 2; ++_i) \
;         __builtin_amdgcn_global_load_lds((const unsigned*)((const char*)(gbase) + (voff)[_i]), (LAS unsigned*)(lds + (bufoff) + ldsw + _i * 8192), 16, 0, 0); } while (0)
; #define PG8_LDA(dst, b, h) do { _Pragma("unroll") for (int m = 0; m < 4; ++m) { if constexpr (F8) dst##8[m] = PG8_LD32(lds + PG8_SA(b, h) + aoff + m * 2048); \
;         else { _Pragma("unroll") for (int k = 0; k < 2; ++k) dst[m][k] = *(const LAS bf16x8*)(lds + PG8_SA(b, h) + aoff + m * 2048 + k * 1024); } } } while (0)
; #define PG8_LDB(dst, b, h) do { _Pragma("unroll") for (int n = 0; n < 2; ++n) { if constexpr (F8) dst##8[n] = PG8_LD32(lds + PG8_SB(b, h) + boff + n * 2048); \
;         else { _Pragma("unroll") for (int k = 0; k < 2; ++k) dst[n][k] = *(const LAS bf16x8*)(lds + PG8_SB(b, h) + boff + n * 2048 + k * 1024); } } } while (0)
; #define PG8_WAIT_V(n) asm volatile("s_waitcnt vmcnt(" #n ")" ::: "memory")
; #define PG8_WAIT_L(n) asm volatile("s_waitcnt lgkmcnt(" #n ")" ::: "memory")
; #define PG8_BAR __builtin_amdgcn_s_barrier()
; #define PG8_SCHED __builtin_amdgcn_sched_barrier(0)
; template <class Epi, class Sched, bool GATHER, bool F8 = false>
; __device__ __forceinline__ void gemm_phase(LAS unsigned char* lds, const int K, const Sched& S, const Epi& E) {
;     ...
;             PG8_LDB(B0, 1, 0); PG8_LDB(B1, 1, 1); PG8_SCHED; PG8_LDA(At, 1, 0); PG8_STAGE(PG8_SA(0, 1), a2, vN[1]);
;             PG8_WAIT_V(8); PG8_WAIT_L(0); PG8_BAR; PG8_MMA(0, 0, At, B0); PG8_MMA(0, 1, At, B1); PG8_BAR; PG8_SCHED;
;             PG8_LDA(At, 1, 1); PG8_STAGE(PG8_SB(1, 0), b3, voffB); PG8_STAGE(PG8_SB(1, 1), b3 + hstepB, voffB); PG8_STAGE(PG8_SA(1, 0), a3, vN[0]);
;             PG8_WAIT_V(8); PG8_WAIT_L(0); PG8_BAR; PG8_MMA(1, 0, At, B0); PG8_MMA(1, 1, At, B1); PG8_BAR; PG8_SCHED;
;         }
;         if (wr == 0) PG8_BAR;
	ds_read_b128 v[2:5], v194
	ds_read_b128 v[6:9], v194 offset:1024
	ds_read_b128 v[10:13], v194 offset:2048
	ds_read_b128 v[14:17], v194 offset:3072
	ds_read_b128 v[18:21], v195
	ds_read_b128 v[22:25], v195 offset:1024
	ds_read_b128 v[26:29], v195 offset:2048
	ds_read_b128 v[30:33], v195 offset:3072
	s_mov_b32 m0, s13
	v_lshl_add_u64 v[228:229], s[44:45], 0, v[166:167]
	ds_read_b128 v[196:199], v193 offset:32768
	ds_read_b128 v[200:203], v193 offset:33792
	ds_read_b128 v[204:207], v193 offset:34816
	ds_read_b128 v[208:211], v193 offset:35840
	ds_read_b128 v[212:215], v193 offset:36864
	ds_read_b128 v[216:219], v193 offset:37888
	ds_read_b128 v[220:223], v193 offset:38912
	ds_read_b128 v[224:227], v193 offset:39936
	global_load_lds_dwordx4 v[228:229], off
	v_lshl_add_u64 v[228:229], s[44:45], 0, v[174:175]
	s_mov_b32 m0, s46
	s_nop 0
	global_load_lds_dwordx4 v[228:229], off
	s_waitcnt vmcnt(8)
	s_waitcnt lgkmcnt(0)
	s_barrier
	s_setprio 1
	v_mfma_scale_f32_16x16x128_f8f6f4 v[158:161], v[2:9], v[196:203], v[158:161], v188, v188 op_sel_hi:[0,0,0]
	v_mfma_scale_f32_16x16x128_f8f6f4 v[154:157], v[10:17], v[196:203], v[154:157], v188, v188 op_sel_hi:[0,0,0]
	v_mfma_scale_f32_16x16x128_f8f6f4 v[142:145], v[2:9], v[204:211], v[142:145], v188, v188 op_sel_hi:[0,0,0]
	v_mfma_scale_f32_16x16x128_f8f6f4 v[138:141], v[10:17], v[204:211], v[138:141], v188, v188 op_sel_hi:[0,0,0]
	v_mfma_scale_f32_16x16x128_f8f6f4 v[126:129], v[2:9], v[212:219], v[126:129], v188, v188 op_sel_hi:[0,0,0]
	v_mfma_scale_f32_16x16x128_f8f6f4 v[122:125], v[10:17], v[212:219], v[122:125], v188, v188 op_sel_hi:[0,0,0]
	v_mfma_scale_f32_16x16x128_f8f6f4 v[110:113], v[2:9], v[220:227], v[110:113], v188, v188 op_sel_hi:[0,0,0]
	v_mfma_scale_f32_16x16x128_f8f6f4 v[106:109], v[10:17], v[220:227], v[106:109], v188, v188 op_sel_hi:[0,0,0]
	s_setprio 0
	s_setprio 1
	v_mfma_scale_f32_16x16x128_f8f6f4 v[150:153], v[18:25], v[196:203], v[150:153], v188, v188 op_sel_hi:[0,0,0]
	v_mfma_scale_f32_16x16x128_f8f6f4 v[146:149], v[26:33], v[196:203], v[146:149], v188, v188 op_sel_hi:[0,0,0]
	v_mfma_scale_f32_16x16x128_f8f6f4 v[134:137], v[18:25], v[204:211], v[134:137], v188, v188 op_sel_hi:[0,0,0]
	v_mfma_scale_f32_16x16x128_f8f6f4 v[130:133], v[26:33], v[204:211], v[130:133], v188, v188 op_sel_hi:[0,0,0]
	v_mfma_scale_f32_16x16x128_f8f6f4 v[118:121], v[18:25], v[212:219], v[118:121], v188, v188 op_sel_hi:[0,0,0]
	v_mfma_scale_f32_16x16x128_f8f6f4 v[114:117], v[26:33], v[212:219], v[114:117], v188, v188 op_sel_hi:[0,0,0]
	v_mfma_scale_f32_16x16x128_f8f6f4 v[102:105], v[18:25], v[220:227], v[102:105], v188, v188 op_sel_hi:[0,0,0]
	v_mfma_scale_f32_16x16x128_f8f6f4 v[98:101], v[26:33], v[220:227], v[98:101], v188, v188 op_sel_hi:[0,0,0]
	s_setprio 0
	s_barrier
	s_mov_b32 m0, s59
	v_lshl_add_u64 v[180:181], v[180:181], 0, s[24:25]
	s_add_u32 s42, s42, 0x10080
	ds_read_b128 v[196:199], v193 offset:49152
	ds_read_b128 v[200:203], v193 offset:50176
	ds_read_b128 v[204:207], v193 offset:51200
	ds_read_b128 v[208:211], v193 offset:52224
	ds_read_b128 v[212:215], v193 offset:53248
	ds_read_b128 v[216:219], v193 offset:54272
	ds_read_b128 v[220:223], v193 offset:55296
	ds_read_b128 v[224:227], v193 offset:56320
	global_load_lds_dwordx4 v[180:181], off
	v_lshl_add_u64 v[180:181], v[182:183], 0, s[24:25]
	s_mov_b32 m0, s60
	s_addc_u32 s43, s43, 0
	global_load_lds_dwordx4 v[180:181], off
	v_lshl_add_u64 v[180:181], s[42:43], 0, v[162:163]
	s_mov_b32 m0, s61
	s_nop 0
	global_load_lds_dwordx4 v[180:181], off
	v_lshl_add_u64 v[180:181], s[42:43], 0, v[168:169]
	s_mov_b32 m0, s62
	s_nop 0
	global_load_lds_dwordx4 v[180:181], off
	v_lshl_add_u64 v[180:181], v[184:185], 0, s[24:25]
	s_mov_b32 m0, s48
	s_nop 0
	global_load_lds_dwordx4 v[180:181], off
	v_lshl_add_u64 v[180:181], v[186:187], 0, s[24:25]
	s_mov_b32 m0, s49
	s_nop 0
	global_load_lds_dwordx4 v[180:181], off
	s_waitcnt vmcnt(8)
	s_waitcnt lgkmcnt(0)
	s_barrier
	s_setprio 1
	v_mfma_scale_f32_16x16x128_f8f6f4 v[94:97], v[2:9], v[196:203], v[94:97], v188, v188 op_sel_hi:[0,0,0]
	v_mfma_scale_f32_16x16x128_f8f6f4 v[90:93], v[10:17], v[196:203], v[90:93], v188, v188 op_sel_hi:[0,0,0]
	v_mfma_scale_f32_16x16x128_f8f6f4 v[78:81], v[2:9], v[204:211], v[78:81], v188, v188 op_sel_hi:[0,0,0]
	v_mfma_scale_f32_16x16x128_f8f6f4 v[74:77], v[10:17], v[204:211], v[74:77], v188, v188 op_sel_hi:[0,0,0]
	v_mfma_scale_f32_16x16x128_f8f6f4 v[62:65], v[2:9], v[212:219], v[62:65], v188, v188 op_sel_hi:[0,0,0]
	v_mfma_scale_f32_16x16x128_f8f6f4 v[58:61], v[10:17], v[212:219], v[58:61], v188, v188 op_sel_hi:[0,0,0]
	v_mfma_scale_f32_16x16x128_f8f6f4 v[46:49], v[2:9], v[220:227], v[46:49], v188, v188 op_sel_hi:[0,0,0]
	v_mfma_scale_f32_16x16x128_f8f6f4 v[42:45], v[10:17], v[220:227], v[42:45], v188, v188 op_sel_hi:[0,0,0]
	s_setprio 0
	s_setprio 1
	v_mfma_scale_f32_16x16x128_f8f6f4 v[86:89], v[18:25], v[196:203], v[86:89], v188, v188 op_sel_hi:[0,0,0]
	v_mfma_scale_f32_16x16x128_f8f6f4 v[82:85], v[26:33], v[196:203], v[82:85], v188, v188 op_sel_hi:[0,0,0]
	v_mfma_scale_f32_16x16x128_f8f6f4 v[70:73], v[18:25], v[204:211], v[70:73], v188, v188 op_sel_hi:[0,0,0]
	v_mfma_scale_f32_16x16x128_f8f6f4 v[66:69], v[26:33], v[204:211], v[66:69], v188, v188 op_sel_hi:[0,0,0]
	v_mfma_scale_f32_16x16x128_f8f6f4 v[54:57], v[18:25], v[212:219], v[54:57], v188, v188 op_sel_hi:[0,0,0]
	v_mfma_scale_f32_16x16x128_f8f6f4 v[50:53], v[26:33], v[212:219], v[50:53], v188, v188 op_sel_hi:[0,0,0]
	v_mfma_scale_f32_16x16x128_f8f6f4 v[38:41], v[18:25], v[220:227], v[38:41], v188, v188 op_sel_hi:[0,0,0]
	v_mfma_scale_f32_16x16x128_f8f6f4 v[34:37], v[26:33], v[220:227], v[34:37], v188, v188 op_sel_hi:[0,0,0]
	s_setprio 0
	s_barrier
	s_add_i32 s52, s52, 2
	s_add_u32 s40, s40, 0x100
	s_addc_u32 s41, s41, 0
	s_cmp_gt_u32 s52, 13
	s_cbranch_scc0 .LBB0_702
	s_cmpk_lt_u32 s3, 0x100
	s_cbranch_scc0 .LBB0_705
	s_barrier

; #define PG8_STAGE(bufoff, gbase, voff) do { _Pragma("unroll") for (int _i = 0; _i < 2; ++_i) \
;         __builtin_amdgcn_global_load_lds((const unsigned*)((const char*)(gbase) + (voff)[_i]), (LAS unsigned*)(lds + (bufoff) + ldsw + _i * 8192), 16, 0, 0); } while (0)
; #define PG8_LDA(dst, b, h) do { _Pragma("unroll") for (int m = 0; m < 4; ++m) { if constexpr (F8) dst##8[m] = PG8_LD32(lds + PG8_SA(b, h) + aoff + m * 2048); \
;         else { _Pragma("unroll") for (int k = 0; k < 2; ++k) dst[m][k] = *(const LAS bf16x8*)(lds + PG8_SA(b, h) + aoff + m * 2048 + k * 1024); } } } while (0)
; #define PG8_LDB(dst, b, h) do { _Pragma("unroll") for (int n = 0; n < 2; ++n) { if constexpr (F8) dst##8[n] = PG8_LD32(lds + PG8_SB(b, h) + boff + n * 2048); \
;         else { _Pragma("unroll") for (int k = 0; k < 2; ++k) dst[n][k] = *(const LAS bf16x8*)(lds + PG8_SB(b, h) + boff + n * 2048 + k * 1024); } } } while (0)
; #define PG8_WAIT_V(n) asm volatile("s_waitcnt vmcnt(" #n ")" ::: "memory")
; #define PG8_WAIT_L(n) asm volatile("s_waitcnt lgkmcnt(" #n ")" ::: "memory")
; #define PG8_BAR __builtin_amdgcn_s_barrier()
; #define PG8_SCHED __builtin_amdgcn_sched_barrier(0)
; template <class Epi, class Sched, bool GATHER, bool F8 = false>
; __device__ __forceinline__ void gemm_phase(LAS unsigned char* lds, const int K, const Sched& S, const Epi& E) {
;     ...
;             if constexpr (GATHER) { if (last && has_next) S.offsets(ui + 1, RA, CA, vN); }
;             PG8_LDB(B0, 0, 0); PG8_LDB(B1, 0, 1); PG8_SCHED; PG8_LDA(At, 0, 0); PG8_STAGE(PG8_SA(1, 1), a1, vA[1]);
;             PG8_WAIT_V(8); PG8_WAIT_L(0); PG8_BAR; PG8_MMA(0, 0, At, B0); PG8_MMA(0, 1, At, B1); PG8_BAR; PG8_SCHED;
;             PG8_LDA(At, 0, 1); PG8_STAGE(PG8_SB(0, 0), b2, voffB); PG8_STAGE(PG8_SB(0, 1), b2 + hstepB, voffB); PG8_STAGE(PG8_SA(0, 0), a2, vN[0]);
;             PG8_WAIT_V(8); PG8_WAIT_L(0); PG8_BAR; PG8_MMA(1, 0, At, B0); PG8_MMA(1, 1, At, B1); PG8_BAR; PG8_SCHED;
.LBB0_1036:
	v_add_u32_e32 v62, s58, v167
	ds_read_b128 v[2:5], v62
	ds_read_b128 v[6:9], v62 offset:1024
	ds_read_b128 v[172:175], v62 offset:2048
	ds_read_b128 v[176:179], v62 offset:3072
	v_add_u32_e32 v62, s59, v167
	ds_read_b128 v[180:183], v62
	ds_read_b128 v[184:187], v62 offset:1024
	ds_read_b128 v[188:191], v62 offset:2048
	ds_read_b128 v[192:195], v62 offset:3072
	s_add_u32 s48, s44, 0x80
	s_addc_u32 s49, s45, 0
	s_and_b64 s[46:47], s[46:47], exec
	s_cselect_b32 s49, s1, s49
	s_cselect_b32 s48, s0, s48
	s_cselect_b32 s47, s41, s66
	s_cselect_b32 s46, s40, s65
	s_mov_b32 m0, s61
	v_lshl_add_u64 v[62:63], s[44:45], 0, v[58:59]
	ds_read_b128 v[196:199], v168
	ds_read_b128 v[200:203], v168 offset:1024
	ds_read_b128 v[204:207], v168 offset:2048
	ds_read_b128 v[208:211], v168 offset:3072
	ds_read_b128 v[212:215], v168 offset:4096
	ds_read_b128 v[216:219], v168 offset:5120
	ds_read_b128 v[220:223], v168 offset:6144
	ds_read_b128 v[224:227], v168 offset:7168
	global_load_lds_dwordx4 v[62:63], off
	v_lshl_add_u64 v[62:63], s[44:45], 0, v[60:61]
	s_mov_b32 m0, s62
	s_nop 0
	global_load_lds_dwordx4 v[62:63], off
	s_waitcnt vmcnt(8)
	s_waitcnt lgkmcnt(0)
	s_barrier
	s_setprio 1
	v_mfma_scale_f32_16x16x128_f8f6f4 v[142:145], v[2:9], v[196:203], v[142:145], v165, v165 op_sel_hi:[0,0,0]
	v_mfma_scale_f32_16x16x128_f8f6f4 v[134:137], v[172:179], v[196:203], v[134:137], v165, v165 op_sel_hi:[0,0,0]
	v_mfma_scale_f32_16x16x128_f8f6f4 v[126:129], v[2:9], v[204:211], v[126:129], v165, v165 op_sel_hi:[0,0,0]
	v_mfma_scale_f32_16x16x128_f8f6f4 v[118:121], v[172:179], v[204:211], v[118:121], v165, v165 op_sel_hi:[0,0,0]
	v_mfma_scale_f32_16x16x128_f8f6f4 v[110:113], v[2:9], v[212:219], v[110:113], v165, v165 op_sel_hi:[0,0,0]
	v_mfma_scale_f32_16x16x128_f8f6f4 v[102:105], v[172:179], v[212:219], v[102:105], v165, v165 op_sel_hi:[0,0,0]
	v_mfma_scale_f32_16x16x128_f8f6f4 v[94:97], v[2:9], v[220:227], v[94:97], v165, v165 op_sel_hi:[0,0,0]
	v_mfma_scale_f32_16x16x128_f8f6f4 v[86:89], v[172:179], v[220:227], v[86:89], v165, v165 op_sel_hi:[0,0,0]
	s_setprio 0
	s_setprio 1
	v_mfma_scale_f32_16x16x128_f8f6f4 v[138:141], v[180:187], v[196:203], v[138:141], v165, v165 op_sel_hi:[0,0,0]
	v_mfma_scale_f32_16x16x128_f8f6f4 v[130:133], v[188:195], v[196:203], v[130:133], v165, v165 op_sel_hi:[0,0,0]
	v_mfma_scale_f32_16x16x128_f8f6f4 v[122:125], v[180:187], v[204:211], v[122:125], v165, v165 op_sel_hi:[0,0,0]
	v_mfma_scale_f32_16x16x128_f8f6f4 v[114:117], v[188:195], v[204:211], v[114:117], v165, v165 op_sel_hi:[0,0,0]
	v_mfma_scale_f32_16x16x128_f8f6f4 v[106:109], v[180:187], v[212:219], v[106:109], v165, v165 op_sel_hi:[0,0,0]
	v_mfma_scale_f32_16x16x128_f8f6f4 v[98:101], v[188:195], v[212:219], v[98:101], v165, v165 op_sel_hi:[0,0,0]
	v_mfma_scale_f32_16x16x128_f8f6f4 v[90:93], v[180:187], v[220:227], v[90:93], v165, v165 op_sel_hi:[0,0,0]
	v_mfma_scale_f32_16x16x128_f8f6f4 v[82:85], v[188:195], v[220:227], v[82:85], v165, v165 op_sel_hi:[0,0,0]
	s_setprio 0
	s_barrier
	s_add_i32 s68, s58, s37
	v_lshl_add_u64 v[62:63], s[46:47], 0, v[148:149]
	s_mov_b32 m0, s68
	ds_read_b128 v[196:199], v168 offset:16384
	ds_read_b128 v[200:203], v168 offset:17408
	ds_read_b128 v[204:207], v168 offset:18432
	ds_read_b128 v[208:211], v168 offset:19456
	ds_read_b128 v[212:215], v168 offset:20480
	ds_read_b128 v[216:219], v168 offset:21504
	ds_read_b128 v[220:223], v168 offset:22528
	ds_read_b128 v[224:227], v168 offset:23552
	global_load_lds_dwordx4 v[62:63], off
	s_add_i32 m0, s68, 0x2000
	s_add_u32 s68, s46, 0x40000
	v_lshl_add_u64 v[64:65], s[46:47], 0, v[146:147]
	s_addc_u32 s69, s47, 0
	s_add_i32 s70, s59, s37
	global_load_lds_dwordx4 v[64:65], off
	v_lshl_add_u64 v[156:157], s[68:69], 0, v[148:149]
	s_mov_b32 m0, s70
	v_mov_b32_e32 v155, v153
	global_load_lds_dwordx4 v[156:157], off
	v_lshl_add_u64 v[156:157], s[68:69], 0, v[146:147]
	s_add_i32 m0, s70, 0x2000
	v_lshl_add_u64 v[158:159], s[48:49], 0, v[152:153]
	global_load_lds_dwordx4 v[156:157], off
	s_mov_b32 m0, s51
	v_lshl_add_u64 v[156:157], s[48:49], 0, v[154:155]
	global_load_lds_dwordx4 v152, s[48:49]
	s_mov_b32 m0, s52
	s_nop 0
	global_load_lds_dwordx4 v154, s[48:49]
	s_waitcnt vmcnt(8)
	s_waitcnt lgkmcnt(0)
	s_barrier
	s_setprio 1
	v_mfma_scale_f32_16x16x128_f8f6f4 v[78:81], v[2:9], v[196:203], v[78:81], v165, v165 op_sel_hi:[0,0,0]
	v_mfma_scale_f32_16x16x128_f8f6f4 v[70:73], v[172:179], v[196:203], v[70:73], v165, v165 op_sel_hi:[0,0,0]
	v_mfma_scale_f32_16x16x128_f8f6f4 v[54:57], v[2:9], v[204:211], v[54:57], v165, v165 op_sel_hi:[0,0,0]
	v_mfma_scale_f32_16x16x128_f8f6f4 v[46:49], v[172:179], v[204:211], v[46:49], v165, v165 op_sel_hi:[0,0,0]
	v_mfma_scale_f32_16x16x128_f8f6f4 v[38:41], v[2:9], v[212:219], v[38:41], v165, v165 op_sel_hi:[0,0,0]
	v_mfma_scale_f32_16x16x128_f8f6f4 v[30:33], v[172:179], v[212:219], v[30:33], v165, v165 op_sel_hi:[0,0,0]
	v_mfma_scale_f32_16x16x128_f8f6f4 v[18:21], v[2:9], v[220:227], v[18:21], v165, v165 op_sel_hi:[0,0,0]
	v_mfma_scale_f32_16x16x128_f8f6f4 v[10:13], v[172:179], v[220:227], v[10:13], v165, v165 op_sel_hi:[0,0,0]
	s_setprio 0
	s_setprio 1
	v_mfma_scale_f32_16x16x128_f8f6f4 v[74:77], v[180:187], v[196:203], v[74:77], v165, v165 op_sel_hi:[0,0,0]
	v_mfma_scale_f32_16x16x128_f8f6f4 v[66:69], v[188:195], v[196:203], v[66:69], v165, v165 op_sel_hi:[0,0,0]
	v_mfma_scale_f32_16x16x128_f8f6f4 v[50:53], v[180:187], v[204:211], v[50:53], v165, v165 op_sel_hi:[0,0,0]
	v_mfma_scale_f32_16x16x128_f8f6f4 v[42:45], v[188:195], v[204:211], v[42:45], v165, v165 op_sel_hi:[0,0,0]
	v_mfma_scale_f32_16x16x128_f8f6f4 v[34:37], v[180:187], v[212:219], v[34:37], v165, v165 op_sel_hi:[0,0,0]
	v_mfma_scale_f32_16x16x128_f8f6f4 v[26:29], v[188:195], v[212:219], v[26:29], v165, v165 op_sel_hi:[0,0,0]
	v_mfma_scale_f32_16x16x128_f8f6f4 v[22:25], v[180:187], v[220:227], v[22:25], v165, v165 op_sel_hi:[0,0,0]
	v_mfma_scale_f32_16x16x128_f8f6f4 v[14:17], v[188:195], v[220:227], v[14:17], v165, v165 op_sel_hi:[0,0,0]
	s_setprio 0
	s_barrier
; #define PG8_STAGE(bufoff, gbase, voff) do { _Pragma("unroll") for (int _i = 0; _i < 2; ++_i) \
;         __builtin_amdgcn_global_load_lds((const unsigned*)((const char*)(gbase) + (voff)[_i]), (LAS unsigned*)(lds + (bufoff) + ldsw + _i * 8192), 16, 0, 0); } while (0)
; #define PG8_LDA(dst, b, h) do { _Pragma("unroll") for (int m = 0; m < 4; ++m) { if constexpr (F8) dst##8[m] = PG8_LD32(lds + PG8_SA(b, h) + aoff + m * 2048); \
;         else { _Pragma("unroll") for (int k = 0; k < 2; ++k) dst[m][k] = *(const LAS bf16x8*)(lds + PG8_SA(b, h) + aoff + m * 2048 + k * 1024); } } } while (0)
; #define PG8_LDB(dst, b, h) do { _Pragma("unroll") for (int n = 0; n < 2; ++n) { if constexpr (F8) dst##8[n] = PG8_LD32(lds + PG8_SB(b, h) + boff + n * 2048); \
;         else { _Pragma("unroll") for (int k = 0; k < 2; ++k) dst[n][k] = *(const LAS bf16x8*)(lds + PG8_SB(b, h) + boff + n * 2048 + k * 1024); } } } while (0)
; #define PG8_WAIT_V(n) asm volatile("s_waitcnt vmcnt(" #n ")" ::: "memory")
; #define PG8_WAIT_L(n) asm volatile("s_waitcnt lgkmcnt(" #n ")" ::: "memory")
; #define PG8_BAR __builtin_amdgcn_s_barrier()
; #define PG8_SCHED __builtin_amdgcn_sched_barrier(0)
; template <class Epi, class Sched, bool GATHER, bool F8 = false>
; __device__ __forceinline__ void gemm_phase(LAS unsigned char* lds, const int K, const Sched& S, const Epi& E) {
;     ...
;             PG8_LDB(B0, 1, 0); PG8_LDB(B1, 1, 1); PG8_SCHED; PG8_LDA(At, 1, 0); PG8_STAGE(PG8_SA(0, 1), a2, vN[1]);
;             PG8_WAIT_V(8); PG8_WAIT_L(0); PG8_BAR; PG8_MMA(0, 0, At, B0); PG8_MMA(0, 1, At, B1); PG8_BAR; PG8_SCHED;
;             PG8_LDA(At, 1, 1); PG8_STAGE(PG8_SB(1, 0), b3, voffB); PG8_STAGE(PG8_SB(1, 1), b3 + hstepB, voffB); PG8_STAGE(PG8_SA(1, 0), a3, vN[0]);
;             PG8_WAIT_V(8); PG8_WAIT_L(0); PG8_BAR; PG8_MMA(1, 0, At, B0); PG8_MMA(1, 1, At, B1); PG8_BAR; PG8_SCHED;
;         }
	s_add_i32 s68, 0, 0x18000
	s_add_i32 s69, 0, 0x1c000
	v_add_u32_e32 v2, s68, v167
	v_add_u32_e32 v155, s69, v167
	ds_read_b128 v[172:175], v2
	ds_read_b128 v[176:179], v2 offset:1024
	ds_read_b128 v[180:183], v2 offset:2048
	ds_read_b128 v[184:187], v2 offset:3072
	ds_read_b128 v[2:5], v155
	ds_read_b128 v[6:9], v155 offset:1024
	ds_read_b128 v[188:191], v155 offset:2048
	ds_read_b128 v[192:195], v155 offset:3072
	s_mov_b32 m0, s53
	ds_read_b128 v[196:199], v168 offset:32768
	ds_read_b128 v[200:203], v168 offset:33792
	ds_read_b128 v[204:207], v168 offset:34816
	ds_read_b128 v[208:211], v168 offset:35840
	ds_read_b128 v[212:215], v168 offset:36864
	ds_read_b128 v[216:219], v168 offset:37888
	ds_read_b128 v[220:223], v168 offset:38912
	ds_read_b128 v[224:227], v168 offset:39936
	global_load_lds_dwordx4 v163, s[48:49]
	s_mov_b32 m0, s54
	s_nop 0
	global_load_lds_dwordx4 v164, s[48:49]
	s_waitcnt vmcnt(8)
	s_waitcnt lgkmcnt(0)
	s_barrier
	s_setprio 1
	v_mfma_scale_f32_16x16x128_f8f6f4 v[142:145], v[172:179], v[196:203], v[142:145], v165, v165 op_sel_hi:[0,0,0]
	v_mfma_scale_f32_16x16x128_f8f6f4 v[134:137], v[180:187], v[196:203], v[134:137], v165, v165 op_sel_hi:[0,0,0]
	v_mfma_scale_f32_16x16x128_f8f6f4 v[126:129], v[172:179], v[204:211], v[126:129], v165, v165 op_sel_hi:[0,0,0]
	v_mfma_scale_f32_16x16x128_f8f6f4 v[118:121], v[180:187], v[204:211], v[118:121], v165, v165 op_sel_hi:[0,0,0]
	v_mfma_scale_f32_16x16x128_f8f6f4 v[110:113], v[172:179], v[212:219], v[110:113], v165, v165 op_sel_hi:[0,0,0]
	v_mfma_scale_f32_16x16x128_f8f6f4 v[102:105], v[180:187], v[212:219], v[102:105], v165, v165 op_sel_hi:[0,0,0]
	v_mfma_scale_f32_16x16x128_f8f6f4 v[94:97], v[172:179], v[220:227], v[94:97], v165, v165 op_sel_hi:[0,0,0]
	v_mfma_scale_f32_16x16x128_f8f6f4 v[86:89], v[180:187], v[220:227], v[86:89], v165, v165 op_sel_hi:[0,0,0]
	s_setprio 0
	s_setprio 1
	v_mfma_scale_f32_16x16x128_f8f6f4 v[138:141], v[2:9], v[196:203], v[138:141], v165, v165 op_sel_hi:[0,0,0]
	v_mfma_scale_f32_16x16x128_f8f6f4 v[130:133], v[188:195], v[196:203], v[130:133], v165, v165 op_sel_hi:[0,0,0]
	v_mfma_scale_f32_16x16x128_f8f6f4 v[122:125], v[2:9], v[204:211], v[122:125], v165, v165 op_sel_hi:[0,0,0]
	v_mfma_scale_f32_16x16x128_f8f6f4 v[114:117], v[188:195], v[204:211], v[114:117], v165, v165 op_sel_hi:[0,0,0]
	v_mfma_scale_f32_16x16x128_f8f6f4 v[106:109], v[2:9], v[212:219], v[106:109], v165, v165 op_sel_hi:[0,0,0]
	v_mfma_scale_f32_16x16x128_f8f6f4 v[98:101], v[188:195], v[212:219], v[98:101], v165, v165 op_sel_hi:[0,0,0]
	v_mfma_scale_f32_16x16x128_f8f6f4 v[90:93], v[2:9], v[220:227], v[90:93], v165, v165 op_sel_hi:[0,0,0]
	v_mfma_scale_f32_16x16x128_f8f6f4 v[82:85], v[188:195], v[220:227], v[82:85], v165, v165 op_sel_hi:[0,0,0]
	s_setprio 0
	s_barrier
	s_add_i32 s48, s68, s37
	v_lshl_add_u64 v[62:63], v[62:63], 0, s[100:101]
	s_mov_b32 m0, s48
	ds_read_b128 v[196:199], v168 offset:49152
	ds_read_b128 v[200:203], v168 offset:50176
	ds_read_b128 v[204:207], v168 offset:51200
	ds_read_b128 v[208:211], v168 offset:52224
	ds_read_b128 v[212:215], v168 offset:53248
	ds_read_b128 v[216:219], v168 offset:54272
	ds_read_b128 v[220:223], v168 offset:55296
	ds_read_b128 v[224:227], v168 offset:56320
	global_load_lds_dwordx4 v[62:63], off
	s_add_i32 m0, s48, 0x2000
	s_add_u32 s46, s46, 0x41000
	v_lshl_add_u64 v[62:63], v[64:65], 0, s[100:101]
	s_addc_u32 s47, s47, 0
	s_add_i32 s48, s69, s37
	global_load_lds_dwordx4 v[62:63], off
	v_lshl_add_u64 v[62:63], s[46:47], 0, v[148:149]
	s_mov_b32 m0, s48
	s_nop 0
	global_load_lds_dwordx4 v[62:63], off
	v_lshl_add_u64 v[62:63], s[46:47], 0, v[146:147]
	s_add_i32 m0, s48, 0x2000
	s_nop 0
	global_load_lds_dwordx4 v[62:63], off
	v_lshl_add_u64 v[62:63], v[158:159], 0, s[14:15]
	s_mov_b32 m0, s55
	s_nop 0
	global_load_lds_dwordx4 v[62:63], off
	v_lshl_add_u64 v[62:63], v[156:157], 0, s[14:15]
	s_mov_b32 m0, s56
	s_nop 0
	global_load_lds_dwordx4 v[62:63], off
	s_waitcnt vmcnt(8)
	s_waitcnt lgkmcnt(0)
	s_barrier
	s_setprio 1
	v_mfma_scale_f32_16x16x128_f8f6f4 v[78:81], v[172:179], v[196:203], v[78:81], v165, v165 op_sel_hi:[0,0,0]
	v_mfma_scale_f32_16x16x128_f8f6f4 v[70:73], v[180:187], v[196:203], v[70:73], v165, v165 op_sel_hi:[0,0,0]
	v_mfma_scale_f32_16x16x128_f8f6f4 v[54:57], v[172:179], v[204:211], v[54:57], v165, v165 op_sel_hi:[0,0,0]
	v_mfma_scale_f32_16x16x128_f8f6f4 v[46:49], v[180:187], v[204:211], v[46:49], v165, v165 op_sel_hi:[0,0,0]
	v_mfma_scale_f32_16x16x128_f8f6f4 v[38:41], v[172:179], v[212:219], v[38:41], v165, v165 op_sel_hi:[0,0,0]
	v_mfma_scale_f32_16x16x128_f8f6f4 v[30:33], v[180:187], v[212:219], v[30:33], v165, v165 op_sel_hi:[0,0,0]
	v_mfma_scale_f32_16x16x128_f8f6f4 v[18:21], v[172:179], v[220:227], v[18:21], v165, v165 op_sel_hi:[0,0,0]
	v_mfma_scale_f32_16x16x128_f8f6f4 v[10:13], v[180:187], v[220:227], v[10:13], v165, v165 op_sel_hi:[0,0,0]
	s_setprio 0
	s_setprio 1
	v_mfma_scale_f32_16x16x128_f8f6f4 v[74:77], v[2:9], v[196:203], v[74:77], v165, v165 op_sel_hi:[0,0,0]
	v_mfma_scale_f32_16x16x128_f8f6f4 v[66:69], v[188:195], v[196:203], v[66:69], v165, v165 op_sel_hi:[0,0,0]
	v_mfma_scale_f32_16x16x128_f8f6f4 v[50:53], v[2:9], v[204:211], v[50:53], v165, v165 op_sel_hi:[0,0,0]
	v_mfma_scale_f32_16x16x128_f8f6f4 v[42:45], v[188:195], v[204:211], v[42:45], v165, v165 op_sel_hi:[0,0,0]
	v_mfma_scale_f32_16x16x128_f8f6f4 v[34:37], v[2:9], v[212:219], v[34:37], v165, v165 op_sel_hi:[0,0,0]
	v_mfma_scale_f32_16x16x128_f8f6f4 v[26:29], v[188:195], v[212:219], v[26:29], v165, v165 op_sel_hi:[0,0,0]
	v_mfma_scale_f32_16x16x128_f8f6f4 v[22:25], v[2:9], v[220:227], v[22:25], v165, v165 op_sel_hi:[0,0,0]
	v_mfma_scale_f32_16x16x128_f8f6f4 v[14:17], v[188:195], v[220:227], v[14:17], v165, v165 op_sel_hi:[0,0,0]
	s_setprio 0
	s_barrier
	s_add_i32 s67, s67, 2
	s_add_u32 s44, s44, 0x100
	s_addc_u32 s45, s45, 0
	s_add_u32 s65, s65, 0x2000
	s_addc_u32 s66, s66, 0
	s_cmp_gt_u32 s67, 13
	s_cbranch_scc1 .LBB0_1039

; #define PG8_STAGE(bufoff, gbase, voff) do { _Pragma("unroll") for (int _i = 0; _i < 2; ++_i) \
;         __builtin_amdgcn_global_load_lds((const unsigned*)((const char*)(gbase) + (voff)[_i]), (LAS unsigned*)(lds + (bufoff) + ldsw + _i * 8192), 16, 0, 0); } while (0)
; #define PG8_LDA(dst, b, h) do { _Pragma("unroll") for (int m = 0; m < 4; ++m) { if constexpr (F8) dst##8[m] = PG8_LD32(lds + PG8_SA(b, h) + aoff + m * 2048); \
;         else { _Pragma("unroll") for (int k = 0; k < 2; ++k) dst[m][k] = *(const LAS bf16x8*)(lds + PG8_SA(b, h) + aoff + m * 2048 + k * 1024); } } } while (0)
; #define PG8_LDB(dst, b, h) do { _Pragma("unroll") for (int n = 0; n < 2; ++n) { if constexpr (F8) dst##8[n] = PG8_LD32(lds + PG8_SB(b, h) + boff + n * 2048); \
;         else { _Pragma("unroll") for (int k = 0; k < 2; ++k) dst[n][k] = *(const LAS bf16x8*)(lds + PG8_SB(b, h) + boff + n * 2048 + k * 1024); } } } while (0)
; #define PG8_WAIT_V(n) asm volatile("s_waitcnt vmcnt(" #n ")" ::: "memory")
; #define PG8_WAIT_L(n) asm volatile("s_waitcnt lgkmcnt(" #n ")" ::: "memory")
; #define PG8_BAR __builtin_amdgcn_s_barrier()
; #define PG8_SCHED __builtin_amdgcn_sched_barrier(0)
; template <class Epi, class Sched, bool GATHER, bool F8 = false>
; __device__ __forceinline__ void gemm_phase(LAS unsigned char* lds, const int K, const Sched& S, const Epi& E) {
;     ...
;             PG8_LDB(B0, 0, 0); PG8_LDB(B1, 0, 1); PG8_SCHED; PG8_LDA(At, 0, 0); PG8_STAGE(PG8_SA(1, 1), a1, vA[1]);
;             PG8_WAIT_V(8); PG8_WAIT_L(0); PG8_BAR; PG8_MMA(0, 0, At, B0); PG8_MMA(0, 1, At, B1); PG8_BAR; PG8_SCHED;
;             PG8_LDA(At, 0, 1); PG8_STAGE(PG8_SB(0, 0), b2, voffB); PG8_STAGE(PG8_SB(0, 1), b2 + hstepB, voffB); PG8_STAGE(PG8_SA(0, 0), a2, vN[0]);
;             PG8_WAIT_V(8); PG8_WAIT_L(0); PG8_BAR; PG8_MMA(1, 0, At, B0); PG8_MMA(1, 1, At, B1); PG8_BAR; PG8_SCHED;
.LBB0_1128:
	v_add_u32_e32 v74, s60, v163
	ds_read_b128 v[2:5], v74
	ds_read_b128 v[6:9], v74 offset:1024
	ds_read_b128 v[172:175], v74 offset:2048
	ds_read_b128 v[176:179], v74 offset:3072
	v_add_u32_e32 v74, s61, v163
	ds_read_b128 v[180:183], v74
	ds_read_b128 v[184:187], v74 offset:1024
	ds_read_b128 v[188:191], v74 offset:2048
	ds_read_b128 v[192:195], v74 offset:3072
	s_add_u32 s46, s44, 0x80
	s_addc_u32 s47, s45, 0
	s_cmp_eq_u32 s18, 12
	s_cselect_b32 s49, s41, s47
	s_cselect_b32 s48, s40, s46
	s_cselect_b32 s47, s43, s13
	s_cselect_b32 s46, s42, s1
	v_lshl_add_u64 v[220:221], s[44:45], 0, v[158:159]
	s_add_i32 m0, s51, 0xc000
	ds_read_b128 v[74:77], v167
	ds_read_b128 v[78:81], v167 offset:1024
	ds_read_b128 v[196:199], v167 offset:2048
	ds_read_b128 v[200:203], v167 offset:3072
	ds_read_b128 v[204:207], v167 offset:4096
	ds_read_b128 v[208:211], v167 offset:5120
	ds_read_b128 v[212:215], v167 offset:6144
	ds_read_b128 v[216:219], v167 offset:7168
	global_load_lds_dwordx4 v[220:221], off
	v_lshl_add_u64 v[220:221], s[44:45], 0, v[160:161]
	s_add_i32 m0, s51, 0xe000
	s_nop 0
	global_load_lds_dwordx4 v[220:221], off
	s_waitcnt vmcnt(8)
	s_waitcnt lgkmcnt(0)
	s_barrier
	s_setprio 1
	v_mfma_scale_f32_16x16x128_f8f6f4 v[142:145], v[2:9], v[74:81], v[142:145], v162, v162 op_sel_hi:[0,0,0]
	v_mfma_scale_f32_16x16x128_f8f6f4 v[138:141], v[172:179], v[74:81], v[138:141], v162, v162 op_sel_hi:[0,0,0]
	v_mfma_scale_f32_16x16x128_f8f6f4 v[126:129], v[2:9], v[196:203], v[126:129], v162, v162 op_sel_hi:[0,0,0]
	v_mfma_scale_f32_16x16x128_f8f6f4 v[122:125], v[172:179], v[196:203], v[122:125], v162, v162 op_sel_hi:[0,0,0]
	v_mfma_scale_f32_16x16x128_f8f6f4 v[110:113], v[2:9], v[204:211], v[110:113], v162, v162 op_sel_hi:[0,0,0]
	v_mfma_scale_f32_16x16x128_f8f6f4 v[106:109], v[172:179], v[204:211], v[106:109], v162, v162 op_sel_hi:[0,0,0]
	v_mfma_scale_f32_16x16x128_f8f6f4 v[94:97], v[2:9], v[212:219], v[94:97], v162, v162 op_sel_hi:[0,0,0]
	v_mfma_scale_f32_16x16x128_f8f6f4 v[90:93], v[172:179], v[212:219], v[90:93], v162, v162 op_sel_hi:[0,0,0]
	s_setprio 0
	s_setprio 1
	v_mfma_scale_f32_16x16x128_f8f6f4 v[134:137], v[180:187], v[74:81], v[134:137], v162, v162 op_sel_hi:[0,0,0]
	v_mfma_scale_f32_16x16x128_f8f6f4 v[130:133], v[188:195], v[74:81], v[130:133], v162, v162 op_sel_hi:[0,0,0]
	v_mfma_scale_f32_16x16x128_f8f6f4 v[118:121], v[180:187], v[196:203], v[118:121], v162, v162 op_sel_hi:[0,0,0]
	v_mfma_scale_f32_16x16x128_f8f6f4 v[114:117], v[188:195], v[196:203], v[114:117], v162, v162 op_sel_hi:[0,0,0]
	v_mfma_scale_f32_16x16x128_f8f6f4 v[102:105], v[180:187], v[204:211], v[102:105], v162, v162 op_sel_hi:[0,0,0]
	v_mfma_scale_f32_16x16x128_f8f6f4 v[98:101], v[188:195], v[204:211], v[98:101], v162, v162 op_sel_hi:[0,0,0]
	v_mfma_scale_f32_16x16x128_f8f6f4 v[86:89], v[180:187], v[212:219], v[86:89], v162, v162 op_sel_hi:[0,0,0]
	v_mfma_scale_f32_16x16x128_f8f6f4 v[82:85], v[188:195], v[212:219], v[82:85], v162, v162 op_sel_hi:[0,0,0]
	s_setprio 0
	s_barrier
	s_add_i32 s65, s60, s25
	v_lshl_add_u64 v[74:75], s[46:47], 0, v[156:157]
	s_mov_b32 m0, s65
	ds_read_b128 v[196:199], v167 offset:16384
	ds_read_b128 v[200:203], v167 offset:17408
	ds_read_b128 v[204:207], v167 offset:18432
	ds_read_b128 v[208:211], v167 offset:19456
	ds_read_b128 v[212:215], v167 offset:20480
	ds_read_b128 v[216:219], v167 offset:21504
	ds_read_b128 v[220:223], v167 offset:22528
	ds_read_b128 v[224:227], v167 offset:23552
	global_load_lds_dwordx4 v[74:75], off
	s_add_i32 m0, s65, 0x2000
	s_add_u32 s66, s46, 0x10000
	v_lshl_add_u64 v[76:77], s[46:47], 0, v[150:151]
	s_addc_u32 s67, s47, 0
	s_add_i32 s65, s61, s25
	global_load_lds_dwordx4 v[76:77], off
	v_lshl_add_u64 v[78:79], s[66:67], 0, v[156:157]
	s_mov_b32 m0, s65
	v_lshl_add_u64 v[80:81], s[48:49], 0, v[146:147]
	global_load_lds_dwordx4 v[78:79], off
	v_lshl_add_u64 v[78:79], s[66:67], 0, v[150:151]
	s_add_i32 m0, s65, 0x2000
	s_nop 0
	global_load_lds_dwordx4 v[78:79], off
	v_lshl_add_u64 v[78:79], s[48:49], 0, v[152:153]
	s_mov_b32 m0, s51
	s_nop 0
	global_load_lds_dwordx4 v[78:79], off
	s_mov_b32 m0, s52
	s_nop 0
	global_load_lds_dwordx4 v[80:81], off
	s_waitcnt vmcnt(8)
	s_waitcnt lgkmcnt(0)
	s_barrier
	s_setprio 1
	v_mfma_scale_f32_16x16x128_f8f6f4 v[70:73], v[2:9], v[196:203], v[70:73], v162, v162 op_sel_hi:[0,0,0]
	v_mfma_scale_f32_16x16x128_f8f6f4 v[66:69], v[172:179], v[196:203], v[66:69], v162, v162 op_sel_hi:[0,0,0]
	v_mfma_scale_f32_16x16x128_f8f6f4 v[54:57], v[2:9], v[204:211], v[54:57], v162, v162 op_sel_hi:[0,0,0]
	v_mfma_scale_f32_16x16x128_f8f6f4 v[50:53], v[172:179], v[204:211], v[50:53], v162, v162 op_sel_hi:[0,0,0]
	v_mfma_scale_f32_16x16x128_f8f6f4 v[38:41], v[2:9], v[212:219], v[38:41], v162, v162 op_sel_hi:[0,0,0]
	v_mfma_scale_f32_16x16x128_f8f6f4 v[34:37], v[172:179], v[212:219], v[34:37], v162, v162 op_sel_hi:[0,0,0]
	v_mfma_scale_f32_16x16x128_f8f6f4 v[18:21], v[2:9], v[220:227], v[18:21], v162, v162 op_sel_hi:[0,0,0]
	v_mfma_scale_f32_16x16x128_f8f6f4 v[22:25], v[172:179], v[220:227], v[22:25], v162, v162 op_sel_hi:[0,0,0]
	s_setprio 0
	s_setprio 1
	v_mfma_scale_f32_16x16x128_f8f6f4 v[62:65], v[180:187], v[196:203], v[62:65], v162, v162 op_sel_hi:[0,0,0]
	v_mfma_scale_f32_16x16x128_f8f6f4 v[58:61], v[188:195], v[196:203], v[58:61], v162, v162 op_sel_hi:[0,0,0]
	v_mfma_scale_f32_16x16x128_f8f6f4 v[46:49], v[180:187], v[204:211], v[46:49], v162, v162 op_sel_hi:[0,0,0]
	v_mfma_scale_f32_16x16x128_f8f6f4 v[42:45], v[188:195], v[204:211], v[42:45], v162, v162 op_sel_hi:[0,0,0]
	v_mfma_scale_f32_16x16x128_f8f6f4 v[30:33], v[180:187], v[212:219], v[30:33], v162, v162 op_sel_hi:[0,0,0]
	v_mfma_scale_f32_16x16x128_f8f6f4 v[26:29], v[188:195], v[212:219], v[26:29], v162, v162 op_sel_hi:[0,0,0]
	v_mfma_scale_f32_16x16x128_f8f6f4 v[10:13], v[180:187], v[220:227], v[10:13], v162, v162 op_sel_hi:[0,0,0]
	v_mfma_scale_f32_16x16x128_f8f6f4 v[14:17], v[188:195], v[220:227], v[14:17], v162, v162 op_sel_hi:[0,0,0]
	s_setprio 0
	s_barrier
; #define PG8_STAGE(bufoff, gbase, voff) do { _Pragma("unroll") for (int _i = 0; _i < 2; ++_i) \
;         __builtin_amdgcn_global_load_lds((const unsigned*)((const char*)(gbase) + (voff)[_i]), (LAS unsigned*)(lds + (bufoff) + ldsw + _i * 8192), 16, 0, 0); } while (0)
; #define PG8_LDA(dst, b, h) do { _Pragma("unroll") for (int m = 0; m < 4; ++m) { if constexpr (F8) dst##8[m] = PG8_LD32(lds + PG8_SA(b, h) + aoff + m * 2048); \
;         else { _Pragma("unroll") for (int k = 0; k < 2; ++k) dst[m][k] = *(const LAS bf16x8*)(lds + PG8_SA(b, h) + aoff + m * 2048 + k * 1024); } } } while (0)
; #define PG8_LDB(dst, b, h) do { _Pragma("unroll") for (int n = 0; n < 2; ++n) { if constexpr (F8) dst##8[n] = PG8_LD32(lds + PG8_SB(b, h) + boff + n * 2048); \
;         else { _Pragma("unroll") for (int k = 0; k < 2; ++k) dst[n][k] = *(const LAS bf16x8*)(lds + PG8_SB(b, h) + boff + n * 2048 + k * 1024); } } } while (0)
; #define PG8_WAIT_V(n) asm volatile("s_waitcnt vmcnt(" #n ")" ::: "memory")
; #define PG8_WAIT_L(n) asm volatile("s_waitcnt lgkmcnt(" #n ")" ::: "memory")
; #define PG8_BAR __builtin_amdgcn_s_barrier()
; #define PG8_SCHED __builtin_amdgcn_sched_barrier(0)
; template <class Epi, class Sched, bool GATHER, bool F8 = false>
; __device__ __forceinline__ void gemm_phase(LAS unsigned char* lds, const int K, const Sched& S, const Epi& E) {
;     ...
;             PG8_LDB(B0, 1, 0); PG8_LDB(B1, 1, 1); PG8_SCHED; PG8_LDA(At, 1, 0); PG8_STAGE(PG8_SA(0, 1), a2, vN[1]);
;             PG8_WAIT_V(8); PG8_WAIT_L(0); PG8_BAR; PG8_MMA(0, 0, At, B0); PG8_MMA(0, 1, At, B1); PG8_BAR; PG8_SCHED;
;             PG8_LDA(At, 1, 1); PG8_STAGE(PG8_SB(1, 0), b3, voffB); PG8_STAGE(PG8_SB(1, 1), b3 + hstepB, voffB); PG8_STAGE(PG8_SA(1, 0), a3, vN[0]);
;             PG8_WAIT_V(8); PG8_WAIT_L(0); PG8_BAR; PG8_MMA(1, 0, At, B0); PG8_MMA(1, 1, At, B1); PG8_BAR; PG8_SCHED;
;         }
;         if (wr == 0) PG8_BAR;
	s_add_i32 s65, 0, 0x18000
	s_add_i32 s66, 0, 0x1c000
	v_add_u32_e32 v2, s65, v163
	v_add_u32_e32 v192, s66, v163
	ds_read_b128 v[172:175], v2
	ds_read_b128 v[176:179], v2 offset:1024
	ds_read_b128 v[180:183], v2 offset:2048
	ds_read_b128 v[184:187], v2 offset:3072
	ds_read_b128 v[2:5], v192
	ds_read_b128 v[6:9], v192 offset:1024
	ds_read_b128 v[188:191], v192 offset:2048
	ds_read_b128 v[192:195], v192 offset:3072
	s_mov_b32 m0, s53
	v_lshl_add_u64 v[228:229], s[48:49], 0, v[154:155]
	ds_read_b128 v[196:199], v167 offset:32768
	ds_read_b128 v[200:203], v167 offset:33792
	ds_read_b128 v[204:207], v167 offset:34816
	ds_read_b128 v[208:211], v167 offset:35840
	ds_read_b128 v[212:215], v167 offset:36864
	ds_read_b128 v[216:219], v167 offset:37888
	ds_read_b128 v[220:223], v167 offset:38912
	ds_read_b128 v[224:227], v167 offset:39936
	global_load_lds_dwordx4 v[228:229], off
	v_lshl_add_u64 v[228:229], s[48:49], 0, v[148:149]
	s_mov_b32 m0, s54
	s_nop 0
	global_load_lds_dwordx4 v[228:229], off
	s_waitcnt vmcnt(8)
	s_waitcnt lgkmcnt(0)
	s_barrier
	s_setprio 1
	v_mfma_scale_f32_16x16x128_f8f6f4 v[142:145], v[172:179], v[196:203], v[142:145], v162, v162 op_sel_hi:[0,0,0]
	v_mfma_scale_f32_16x16x128_f8f6f4 v[138:141], v[180:187], v[196:203], v[138:141], v162, v162 op_sel_hi:[0,0,0]
	v_mfma_scale_f32_16x16x128_f8f6f4 v[126:129], v[172:179], v[204:211], v[126:129], v162, v162 op_sel_hi:[0,0,0]
	v_mfma_scale_f32_16x16x128_f8f6f4 v[122:125], v[180:187], v[204:211], v[122:125], v162, v162 op_sel_hi:[0,0,0]
	v_mfma_scale_f32_16x16x128_f8f6f4 v[110:113], v[172:179], v[212:219], v[110:113], v162, v162 op_sel_hi:[0,0,0]
	v_mfma_scale_f32_16x16x128_f8f6f4 v[106:109], v[180:187], v[212:219], v[106:109], v162, v162 op_sel_hi:[0,0,0]
	v_mfma_scale_f32_16x16x128_f8f6f4 v[94:97], v[172:179], v[220:227], v[94:97], v162, v162 op_sel_hi:[0,0,0]
	v_mfma_scale_f32_16x16x128_f8f6f4 v[90:93], v[180:187], v[220:227], v[90:93], v162, v162 op_sel_hi:[0,0,0]
	s_setprio 0
	s_setprio 1
	v_mfma_scale_f32_16x16x128_f8f6f4 v[134:137], v[2:9], v[196:203], v[134:137], v162, v162 op_sel_hi:[0,0,0]
	v_mfma_scale_f32_16x16x128_f8f6f4 v[130:133], v[188:195], v[196:203], v[130:133], v162, v162 op_sel_hi:[0,0,0]
	v_mfma_scale_f32_16x16x128_f8f6f4 v[118:121], v[2:9], v[204:211], v[118:121], v162, v162 op_sel_hi:[0,0,0]
	v_mfma_scale_f32_16x16x128_f8f6f4 v[114:117], v[188:195], v[204:211], v[114:117], v162, v162 op_sel_hi:[0,0,0]
	v_mfma_scale_f32_16x16x128_f8f6f4 v[102:105], v[2:9], v[212:219], v[102:105], v162, v162 op_sel_hi:[0,0,0]
	v_mfma_scale_f32_16x16x128_f8f6f4 v[98:101], v[188:195], v[212:219], v[98:101], v162, v162 op_sel_hi:[0,0,0]
	v_mfma_scale_f32_16x16x128_f8f6f4 v[86:89], v[2:9], v[220:227], v[86:89], v162, v162 op_sel_hi:[0,0,0]
	v_mfma_scale_f32_16x16x128_f8f6f4 v[82:85], v[188:195], v[220:227], v[82:85], v162, v162 op_sel_hi:[0,0,0]
	s_setprio 0
	s_barrier
	s_add_i32 s48, s65, s25
	v_lshl_add_u64 v[74:75], v[74:75], 0, s[100:101]
	s_mov_b32 m0, s48
	ds_read_b128 v[196:199], v167 offset:49152
	ds_read_b128 v[200:203], v167 offset:50176
	ds_read_b128 v[204:207], v167 offset:51200
	ds_read_b128 v[208:211], v167 offset:52224
	ds_read_b128 v[212:215], v167 offset:53248
	ds_read_b128 v[216:219], v167 offset:54272
	ds_read_b128 v[220:223], v167 offset:55296
	ds_read_b128 v[224:227], v167 offset:56320
	global_load_lds_dwordx4 v[74:75], off
	s_add_i32 m0, s48, 0x2000
	s_add_u32 s46, s46, 0x11000
	v_lshl_add_u64 v[74:75], v[76:77], 0, s[100:101]
	s_addc_u32 s47, s47, 0
	s_add_i32 s48, s66, s25
	global_load_lds_dwordx4 v[74:75], off
	v_lshl_add_u64 v[74:75], s[46:47], 0, v[156:157]
	s_mov_b32 m0, s48
	s_nop 0
	global_load_lds_dwordx4 v[74:75], off
	v_lshl_add_u64 v[74:75], s[46:47], 0, v[150:151]
	s_add_i32 m0, s48, 0x2000
	s_nop 0
	global_load_lds_dwordx4 v[74:75], off
	v_lshl_add_u64 v[74:75], v[78:79], 0, s[16:17]
	s_mov_b32 m0, s56
	s_nop 0
	global_load_lds_dwordx4 v[74:75], off
	v_lshl_add_u64 v[74:75], v[80:81], 0, s[16:17]
	s_mov_b32 m0, s57
	s_nop 0
	global_load_lds_dwordx4 v[74:75], off
	s_waitcnt vmcnt(8)
	s_waitcnt lgkmcnt(0)
	s_barrier
	s_setprio 1
	v_mfma_scale_f32_16x16x128_f8f6f4 v[70:73], v[172:179], v[196:203], v[70:73], v162, v162 op_sel_hi:[0,0,0]
	v_mfma_scale_f32_16x16x128_f8f6f4 v[66:69], v[180:187], v[196:203], v[66:69], v162, v162 op_sel_hi:[0,0,0]
	v_mfma_scale_f32_16x16x128_f8f6f4 v[54:57], v[172:179], v[204:211], v[54:57], v162, v162 op_sel_hi:[0,0,0]
	v_mfma_scale_f32_16x16x128_f8f6f4 v[50:53], v[180:187], v[204:211], v[50:53], v162, v162 op_sel_hi:[0,0,0]
	v_mfma_scale_f32_16x16x128_f8f6f4 v[38:41], v[172:179], v[212:219], v[38:41], v162, v162 op_sel_hi:[0,0,0]
	v_mfma_scale_f32_16x16x128_f8f6f4 v[34:37], v[180:187], v[212:219], v[34:37], v162, v162 op_sel_hi:[0,0,0]
	v_mfma_scale_f32_16x16x128_f8f6f4 v[18:21], v[172:179], v[220:227], v[18:21], v162, v162 op_sel_hi:[0,0,0]
	v_mfma_scale_f32_16x16x128_f8f6f4 v[22:25], v[180:187], v[220:227], v[22:25], v162, v162 op_sel_hi:[0,0,0]
	s_setprio 0
	s_setprio 1
	v_mfma_scale_f32_16x16x128_f8f6f4 v[62:65], v[2:9], v[196:203], v[62:65], v162, v162 op_sel_hi:[0,0,0]
	v_mfma_scale_f32_16x16x128_f8f6f4 v[58:61], v[188:195], v[196:203], v[58:61], v162, v162 op_sel_hi:[0,0,0]
	v_mfma_scale_f32_16x16x128_f8f6f4 v[46:49], v[2:9], v[204:211], v[46:49], v162, v162 op_sel_hi:[0,0,0]
	v_mfma_scale_f32_16x16x128_f8f6f4 v[42:45], v[188:195], v[204:211], v[42:45], v162, v162 op_sel_hi:[0,0,0]
	v_mfma_scale_f32_16x16x128_f8f6f4 v[30:33], v[2:9], v[212:219], v[30:33], v162, v162 op_sel_hi:[0,0,0]
	v_mfma_scale_f32_16x16x128_f8f6f4 v[26:29], v[188:195], v[212:219], v[26:29], v162, v162 op_sel_hi:[0,0,0]
	v_mfma_scale_f32_16x16x128_f8f6f4 v[10:13], v[2:9], v[220:227], v[10:13], v162, v162 op_sel_hi:[0,0,0]
	v_mfma_scale_f32_16x16x128_f8f6f4 v[14:17], v[188:195], v[220:227], v[14:17], v162, v162 op_sel_hi:[0,0,0]
	s_setprio 0
	s_barrier
	s_add_i32 s18, s18, 2
	s_add_u32 s44, s44, 0x100
	s_addc_u32 s45, s45, 0
	s_add_u32 s1, s1, 0x2000
	s_addc_u32 s13, s13, 0
	s_cmp_gt_u32 s18, 13
	s_cbranch_scc0 .LBB0_1128
	s_and_b64 vcc, exec, s[20:21]
	s_cbranch_vccz .LBB0_1131
	s_barrier
